# P10: per-token U-step / gate / V-step vectors kept in a per-wave LDS slot, read per step with ds_read_b32 (no first/second-half v_cndmask selects, no gate mask, no ds_bpermute): 5 VALU fewer per 32-ex
# baseline (speedup 1.0000x reference)
; #define EXP_ROW(src, l) (*(const u32x4*)(UV + ((unsigned)__builtin_amdgcn_readlane((src), (l)) * 1024u + lo16)))
; #define EXP_XROW(tt) do { const char* g_ = (const char*)(xin + (size_t)(tt) * 1024) + lane * 16; LAS unsigned char* l_ = xslot + ((tt) & 1) * 2048; \
;         __builtin_amdgcn_global_load_lds((const unsigned*)g_, (LAS unsigned*)l_, 16, 0, 2); __builtin_amdgcn_global_load_lds((const unsigned*)(g_ + 1024), (LAS unsigned*)(l_ + 1024), 16, 0, 2); } while (0)
; __device__ __forceinline__ void expert_tokens(const unsigned char* __restrict__ UV, const float* __restrict__ US, const float* __restrict__ VS, ...
;     if (t0 >= t1) return;
;     const unsigned lo16 = (unsigned)lane * 16u;
;     const int el = ((lane >> 5) & 1) * 8 + ((lane >> 4) & 1) * 4 + ((lane >> 1) & 1) * 2 + (lane & 1);
;     const unsigned cw0 = (unsigned)IDX[(size_t)t0 * 128 + lane], cw1 = (unsigned)IDX[(size_t)t0 * 128 + 64 + lane];
;     int ci0 = (int)cw0 & rmask, ci1 = (int)cw1 & rmask;
;     float cg0 = __uint_as_float(cw0 & 0xFFFF0000u), cg1 = __uint_as_float(cw1 & 0xFFFF0000u);
;     float csu0 = US[ci0], csu1 = US[ci1], csv0 = VS[ci0], csv1 = VS[ci1];
;     ...
;     EXP_XROW(t0);
;     u32x4 A[EB], B[EB];
; #pragma unroll
;     for (int e = 0; e < EB; ++e) A[e] = EXP_ROW(ci0, e);
; #pragma unroll
;     for (int e = 0; e < EB; ++e) B[e] = EXP_ROW(ci0, EB + e);
.LBB0_1011:
	s_or_b64 exec, exec, s[12:13]
	s_waitcnt lgkmcnt(0)
	s_mul_i32 s8, s24, s96
	s_add_i32 s0, s8, s24
	s_min_i32 s17, s0, 0x8000
	s_sub_i32 s84, s96, s95
	s_add_i32 s84, s84, 8
	s_mul_i32 s84, s84, s24
	s_cmp_le_i32 s84, 0x8000
	s_cselect_b32 s84, 1, 0
	s_cmp_ge_i32 s8, s17
	s_waitcnt vmcnt(0)
	s_barrier
	s_cbranch_scc1 .LBB0_1025
	s_add_u32 s0, s6, 0xf800000
	s_addc_u32 s1, s7, 0
	s_add_u32 s10, s6, 0x1200000
	s_addc_u32 s11, s7, 0
	s_mov_b32 s80, s10
	s_and_b32 s81, s11, 0xffff
	s_mov_b32 s82, 0x1000000
	s_mov_b32 s83, 0x20000
	s_mov_b32 s32, 0xf000f0
	s_lshl_b32 s94, s95, 11
	s_add_i32 s94, s94, 0x10000
	s_lshl_b32 s92, s96, 10
	s_add_u32 s86, s6, s92
	s_addc_u32 s87, s7, 0
	s_add_u32 s86, s86, 0x3500000
	s_addc_u32 s87, s87, 0
	s_add_u32 s88, s86, 0x200
	s_addc_u32 s89, s87, 0
	s_add_u32 s12, s6, 0x1100000
	s_addc_u32 s13, s7, 0
	s_add_u32 s14, s6, 0x1140000
	s_addc_u32 s15, s7, 0
	s_lshl_b32 s2, s95, 12
	s_add_i32 s26, s2, 0
	s_add_u32 s2, s6, 0x1b800000
	s_addc_u32 s3, s7, 0
	s_ashr_i32 s9, s8, 31
	s_lshl_b64 s[6:7], s[8:9], 9
	v_and_b32_e32 v74, 63, v0
	s_add_u32 s6, s0, s6
	s_addc_u32 s7, s1, s7
	v_lshlrev_b32_e32 v192, 2, v74
	global_load_dword v229, v192, s[6:7]
	global_load_dword v230, v192, s[6:7] offset:256
	s_lshl_b64 s[18:19], s[8:9], 11
	s_add_u32 s18, s2, s18
	s_addc_u32 s19, s3, s19
	s_lshl_b32 s9, s8, 11
	v_mov_b32_e32 v1, 0
	s_and_b32 s9, s9, 0x800
	v_lshlrev_b32_e32 v194, 4, v74
	v_mov_b32_e32 v195, v1
	s_add_i32 s9, s26, s9
	s_mov_b64 s[6:7], 0x400
	v_lshl_add_u64 v[2:3], s[18:19], 0, v[194:195]
	s_add_i32 m0, s9, 0x4000
	v_lshl_add_u64 v[2:3], v[2:3], 0, s[6:7]
	global_load_lds_dwordx4 v194, s[18:19] nt
	s_add_i32 m0, s9, 0x4400
	v_mov_b32_e32 v193, v1
	global_load_lds_dwordx4 v[2:3], off nt
	v_and_b32_e32 v77, 2, v0
	v_lshl_add_u64 v[196:197], s[0:1], 0, v[192:193]
	v_lshl_add_u64 v[198:199], s[2:3], 0, v[194:195]
	v_cmp_eq_u32_e64 s[0:1], 0, v77
	v_lshl_add_u64 v[200:201], s[4:5], 0, v[194:195]
	v_lshl_add_u32 v195, v74, 3, s26
	v_mov_b32_e32 v226, 0x358637bd
	v_mov_b32_e32 v227, 0xbf3a00e3
	s_waitcnt vmcnt(0)
	v_alignbit_b32 v229, v229, v229, 16
	v_alignbit_b32 v230, v230, v230, 16
	s_nop 1
	s_mov_b32 s58, 0x99999999
	s_mov_b32 s59, 0x99999999
	v_min_u32_dpp v202, v229, v229 quad_perm:[1,0,3,2] row_mask:0xf bank_mask:0xf
	v_max_u32_dpp v203, v229, v229 quad_perm:[1,0,3,2] row_mask:0xf bank_mask:0xf
	v_min_u32_dpp v204, v230, v230 quad_perm:[1,0,3,2] row_mask:0xf bank_mask:0xf
	v_max_u32_dpp v205, v230, v230 quad_perm:[1,0,3,2] row_mask:0xf bank_mask:0xf
	v_cndmask_b32_e64 v229, v203, v202, s[58:59]
	v_cndmask_b32_e64 v230, v205, v204, s[58:59]
	s_mov_b32 s58, 0xcc33cc33
	s_mov_b32 s59, 0xcc33cc33
	v_min_u32_dpp v202, v229, v229 quad_perm:[2,3,0,1] row_mask:0xf bank_mask:0xf
	v_max_u32_dpp v203, v229, v229 quad_perm:[2,3,0,1] row_mask:0xf bank_mask:0xf
	v_min_u32_dpp v204, v230, v230 quad_perm:[2,3,0,1] row_mask:0xf bank_mask:0xf
	v_max_u32_dpp v205, v230, v230 quad_perm:[2,3,0,1] row_mask:0xf bank_mask:0xf
	v_cndmask_b32_e64 v229, v203, v202, s[58:59]
	v_cndmask_b32_e64 v230, v205, v204, s[58:59]
	s_mov_b32 s58, 0xaa55aa55
	s_mov_b32 s59, 0xaa55aa55
	v_min_u32_dpp v202, v229, v229 quad_perm:[1,0,3,2] row_mask:0xf bank_mask:0xf
	v_max_u32_dpp v203, v229, v229 quad_perm:[1,0,3,2] row_mask:0xf bank_mask:0xf
	v_min_u32_dpp v204, v230, v230 quad_perm:[1,0,3,2] row_mask:0xf bank_mask:0xf
	v_max_u32_dpp v205, v230, v230 quad_perm:[1,0,3,2] row_mask:0xf bank_mask:0xf
	v_cndmask_b32_e64 v229, v203, v202, s[58:59]
	v_cndmask_b32_e64 v230, v205, v204, s[58:59]
	s_mov_b32 s58, 0xf00ff00f
	s_mov_b32 s59, 0xf00ff00f
	v_min_u32_dpp v202, v229, v229 row_ror:8 row_mask:0xf bank_mask:0xf
	v_max_u32_dpp v203, v229, v229 row_ror:8 row_mask:0xf bank_mask:0xf
	v_min_u32_dpp v204, v230, v230 row_ror:8 row_mask:0xf bank_mask:0xf
	v_max_u32_dpp v205, v230, v230 row_ror:8 row_mask:0xf bank_mask:0xf
	v_cndmask_b32_e64 v229, v203, v202, s[58:59]
	v_cndmask_b32_e64 v230, v205, v204, s[58:59]
	s_mov_b32 s58, 0xc3c3c3c3
	s_mov_b32 s59, 0xc3c3c3c3
	v_min_u32_dpp v202, v229, v229 quad_perm:[2,3,0,1] row_mask:0xf bank_mask:0xf
	v_max_u32_dpp v203, v229, v229 quad_perm:[2,3,0,1] row_mask:0xf bank_mask:0xf
	v_min_u32_dpp v204, v230, v230 quad_perm:[2,3,0,1] row_mask:0xf bank_mask:0xf
	v_max_u32_dpp v205, v230, v230 quad_perm:[2,3,0,1] row_mask:0xf bank_mask:0xf
	v_cndmask_b32_e64 v229, v203, v202, s[58:59]
	v_cndmask_b32_e64 v230, v205, v204, s[58:59]
	s_mov_b32 s58, 0xa5a5a5a5
	s_mov_b32 s59, 0xa5a5a5a5
	v_min_u32_dpp v202, v229, v229 quad_perm:[1,0,3,2] row_mask:0xf bank_mask:0xf
	v_max_u32_dpp v203, v229, v229 quad_perm:[1,0,3,2] row_mask:0xf bank_mask:0xf
	v_min_u32_dpp v204, v230, v230 quad_perm:[1,0,3,2] row_mask:0xf bank_mask:0xf
	v_max_u32_dpp v205, v230, v230 quad_perm:[1,0,3,2] row_mask:0xf bank_mask:0xf
	v_cndmask_b32_e64 v229, v203, v202, s[58:59]
	v_cndmask_b32_e64 v230, v205, v204, s[58:59]
	s_mov_b32 s58, 0xf0f00f0f
	s_mov_b32 s59, 0xf0f00f0f
	v_mov_b32_dpp v202, v229 row_half_mirror row_mask:0xf bank_mask:0xf
	v_mov_b32_dpp v204, v230 row_half_mirror row_mask:0xf bank_mask:0xf
	s_nop 0
	v_max_u32_dpp v203, v202, v229 quad_perm:[3,2,1,0] row_mask:0xf bank_mask:0xf
	v_max_u32_dpp v205, v204, v230 quad_perm:[3,2,1,0] row_mask:0xf bank_mask:0xf
	v_min_u32_dpp v202, v202, v229 quad_perm:[3,2,1,0] row_mask:0xf bank_mask:0xf
	v_min_u32_dpp v204, v204, v230 quad_perm:[3,2,1,0] row_mask:0xf bank_mask:0xf
	v_cndmask_b32_e64 v229, v203, v202, s[58:59]
	v_cndmask_b32_e64 v230, v205, v204, s[58:59]
	s_mov_b32 s58, 0xff0000ff
	s_mov_b32 s59, 0xff0000ff
	v_min_u32_dpp v202, v229, v229 row_ror:8 row_mask:0xf bank_mask:0xf
; __device__ __forceinline__ void expert_tokens(const unsigned char* __restrict__ UV, const float* __restrict__ US, const float* __restrict__ VS, ...
;     ...
;     const unsigned cw0 = (unsigned)IDX[(size_t)t0 * 128 + lane], cw1 = (unsigned)IDX[(size_t)t0 * 128 + 64 + lane];
;     int ci0 = (int)cw0 & rmask, ci1 = (int)cw1 & rmask;
;     float cg0 = __uint_as_float(cw0 & 0xFFFF0000u), cg1 = __uint_as_float(cw1 & 0xFFFF0000u);
;     float csu0 = US[ci0], csu1 = US[ci1], csv0 = VS[ci0], csv1 = VS[ci1];
	v_max_u32_dpp v203, v229, v229 row_ror:8 row_mask:0xf bank_mask:0xf
	v_min_u32_dpp v204, v230, v230 row_ror:8 row_mask:0xf bank_mask:0xf
	v_max_u32_dpp v205, v230, v230 row_ror:8 row_mask:0xf bank_mask:0xf
	v_cndmask_b32_e64 v229, v203, v202, s[58:59]
	v_cndmask_b32_e64 v230, v205, v204, s[58:59]
	s_mov_b32 s58, 0xcccc3333
	s_mov_b32 s59, 0xcccc3333
	v_min_u32_dpp v202, v229, v229 quad_perm:[2,3,0,1] row_mask:0xf bank_mask:0xf
	v_max_u32_dpp v203, v229, v229 quad_perm:[2,3,0,1] row_mask:0xf bank_mask:0xf
	v_min_u32_dpp v204, v230, v230 quad_perm:[2,3,0,1] row_mask:0xf bank_mask:0xf
	v_max_u32_dpp v205, v230, v230 quad_perm:[2,3,0,1] row_mask:0xf bank_mask:0xf
	v_cndmask_b32_e64 v229, v203, v202, s[58:59]
	v_cndmask_b32_e64 v230, v205, v204, s[58:59]
	s_mov_b32 s58, 0xaaaa5555
	s_mov_b32 s59, 0xaaaa5555
	v_min_u32_dpp v202, v229, v229 quad_perm:[1,0,3,2] row_mask:0xf bank_mask:0xf
	v_max_u32_dpp v203, v229, v229 quad_perm:[1,0,3,2] row_mask:0xf bank_mask:0xf
	v_min_u32_dpp v204, v230, v230 quad_perm:[1,0,3,2] row_mask:0xf bank_mask:0xf
	v_max_u32_dpp v205, v230, v230 quad_perm:[1,0,3,2] row_mask:0xf bank_mask:0xf
	v_cndmask_b32_e64 v229, v203, v202, s[58:59]
	v_cndmask_b32_e64 v230, v205, v204, s[58:59]
	s_nop 1
	v_permlane16_swap_b32_e32 v229, v230
	s_mov_b32 s58, -1
	s_mov_b32 s59, 0
	v_min_u32_e32 v202, v229, v230
	v_max_u32_e32 v203, v229, v230
	v_cndmask_b32_e64 v229, v203, v202, s[58:59]
	v_cndmask_b32_e64 v230, v202, v203, s[58:59]
	s_mov_b32 s58, 0xf0f0f0f
	s_mov_b32 s59, 0xf0f0f0f0
	v_mov_b32_dpp v202, v229 row_half_mirror row_mask:0xf bank_mask:0xf
	v_mov_b32_dpp v204, v230 row_half_mirror row_mask:0xf bank_mask:0xf
	s_nop 0
	v_max_u32_dpp v203, v202, v229 quad_perm:[3,2,1,0] row_mask:0xf bank_mask:0xf
	v_max_u32_dpp v205, v204, v230 quad_perm:[3,2,1,0] row_mask:0xf bank_mask:0xf
	v_min_u32_dpp v202, v202, v229 quad_perm:[3,2,1,0] row_mask:0xf bank_mask:0xf
	v_min_u32_dpp v204, v204, v230 quad_perm:[3,2,1,0] row_mask:0xf bank_mask:0xf
	v_cndmask_b32_e64 v229, v203, v202, s[58:59]
	v_cndmask_b32_e64 v230, v205, v204, s[58:59]
	s_mov_b32 s58, 0xff00ff
	s_mov_b32 s59, 0xff00ff00
	v_min_u32_dpp v202, v229, v229 row_ror:8 row_mask:0xf bank_mask:0xf
	v_max_u32_dpp v203, v229, v229 row_ror:8 row_mask:0xf bank_mask:0xf
	v_min_u32_dpp v204, v230, v230 row_ror:8 row_mask:0xf bank_mask:0xf
	v_max_u32_dpp v205, v230, v230 row_ror:8 row_mask:0xf bank_mask:0xf
	v_cndmask_b32_e64 v229, v203, v202, s[58:59]
	v_cndmask_b32_e64 v230, v205, v204, s[58:59]
	s_mov_b32 s58, 0x33333333
	s_mov_b32 s59, 0xcccccccc
	v_min_u32_dpp v202, v229, v229 quad_perm:[2,3,0,1] row_mask:0xf bank_mask:0xf
	v_max_u32_dpp v203, v229, v229 quad_perm:[2,3,0,1] row_mask:0xf bank_mask:0xf
	v_min_u32_dpp v204, v230, v230 quad_perm:[2,3,0,1] row_mask:0xf bank_mask:0xf
	v_max_u32_dpp v205, v230, v230 quad_perm:[2,3,0,1] row_mask:0xf bank_mask:0xf
	v_cndmask_b32_e64 v229, v203, v202, s[58:59]
	v_cndmask_b32_e64 v230, v205, v204, s[58:59]
	s_mov_b32 s58, 0x55555555
	s_mov_b32 s59, 0xaaaaaaaa
	v_min_u32_dpp v202, v229, v229 quad_perm:[1,0,3,2] row_mask:0xf bank_mask:0xf
	v_max_u32_dpp v203, v229, v229 quad_perm:[1,0,3,2] row_mask:0xf bank_mask:0xf
	v_min_u32_dpp v204, v230, v230 quad_perm:[1,0,3,2] row_mask:0xf bank_mask:0xf
	v_max_u32_dpp v205, v230, v230 quad_perm:[1,0,3,2] row_mask:0xf bank_mask:0xf
	v_cndmask_b32_e64 v229, v203, v202, s[58:59]
	v_cndmask_b32_e64 v230, v205, v204, s[58:59]
	s_nop 1
	v_permlane32_swap_b32_e32 v229, v230
	s_mov_b32 s58, 0xffff
	s_mov_b32 s59, 0xffff
	v_min_u32_e32 v202, v229, v230
	v_max_u32_e32 v203, v229, v230
	v_cndmask_b32_e64 v229, v203, v202, s[58:59]
	v_cndmask_b32_e64 v230, v202, v203, s[58:59]
	s_nop 1
	v_permlane32_swap_b32_e32 v229, v230
	s_mov_b32 s58, 0xffff
	s_mov_b32 s59, 0xffff
	v_min_u32_e32 v202, v229, v230
	v_max_u32_e32 v203, v229, v230
	v_cndmask_b32_e64 v229, v203, v202, s[58:59]
	v_cndmask_b32_e64 v230, v202, v203, s[58:59]
	s_mov_b32 s58, 0xf0f00f0f
	s_mov_b32 s59, 0xf0f00f0f
	v_mov_b32_dpp v202, v229 row_half_mirror row_mask:0xf bank_mask:0xf
	v_mov_b32_dpp v204, v230 row_half_mirror row_mask:0xf bank_mask:0xf
	s_nop 0
	v_max_u32_dpp v203, v202, v229 quad_perm:[3,2,1,0] row_mask:0xf bank_mask:0xf
	v_max_u32_dpp v205, v204, v230 quad_perm:[3,2,1,0] row_mask:0xf bank_mask:0xf
	v_min_u32_dpp v202, v202, v229 quad_perm:[3,2,1,0] row_mask:0xf bank_mask:0xf
	v_min_u32_dpp v204, v204, v230 quad_perm:[3,2,1,0] row_mask:0xf bank_mask:0xf
	v_cndmask_b32_e64 v229, v203, v202, s[58:59]
	v_cndmask_b32_e64 v230, v205, v204, s[58:59]
	s_mov_b32 s58, 0xff0000ff
	s_mov_b32 s59, 0xff0000ff
	v_min_u32_dpp v202, v229, v229 row_ror:8 row_mask:0xf bank_mask:0xf
	v_max_u32_dpp v203, v229, v229 row_ror:8 row_mask:0xf bank_mask:0xf
	v_min_u32_dpp v204, v230, v230 row_ror:8 row_mask:0xf bank_mask:0xf
	v_max_u32_dpp v205, v230, v230 row_ror:8 row_mask:0xf bank_mask:0xf
	v_cndmask_b32_e64 v229, v203, v202, s[58:59]
	v_cndmask_b32_e64 v230, v205, v204, s[58:59]
	s_mov_b32 s58, 0xcccc3333
	s_mov_b32 s59, 0xcccc3333
	v_min_u32_dpp v202, v229, v229 quad_perm:[2,3,0,1] row_mask:0xf bank_mask:0xf
	v_max_u32_dpp v203, v229, v229 quad_perm:[2,3,0,1] row_mask:0xf bank_mask:0xf
	v_min_u32_dpp v204, v230, v230 quad_perm:[2,3,0,1] row_mask:0xf bank_mask:0xf
	v_max_u32_dpp v205, v230, v230 quad_perm:[2,3,0,1] row_mask:0xf bank_mask:0xf
	v_cndmask_b32_e64 v229, v203, v202, s[58:59]
	v_cndmask_b32_e64 v230, v205, v204, s[58:59]
	s_mov_b32 s58, 0xaaaa5555
	s_mov_b32 s59, 0xaaaa5555
	v_min_u32_dpp v202, v229, v229 quad_perm:[1,0,3,2] row_mask:0xf bank_mask:0xf
	v_max_u32_dpp v203, v229, v229 quad_perm:[1,0,3,2] row_mask:0xf bank_mask:0xf
; #define EXP_ROW(src, l) (*(const u32x4*)(UV + ((unsigned)__builtin_amdgcn_readlane((src), (l)) * 1024u + lo16)))
; #define EXP_XROW(tt) do { const char* g_ = (const char*)(xin + (size_t)(tt) * 1024) + lane * 16; LAS unsigned char* l_ = xslot + ((tt) & 1) * 2048; \
;         __builtin_amdgcn_global_load_lds((const unsigned*)g_, (LAS unsigned*)l_, 16, 0, 2); __builtin_amdgcn_global_load_lds((const unsigned*)(g_ + 1024), (LAS unsigned*)(l_ + 1024), 16, 0, 2); } while (0)
; __device__ __forceinline__ void expert_tokens(const unsigned char* __restrict__ UV, const float* __restrict__ US, const float* __restrict__ VS, ...
;     ...
;     const unsigned cw0 = (unsigned)IDX[(size_t)t0 * 128 + lane], cw1 = (unsigned)IDX[(size_t)t0 * 128 + 64 + lane];
;     int ci0 = (int)cw0 & rmask, ci1 = (int)cw1 & rmask;
;     float cg0 = __uint_as_float(cw0 & 0xFFFF0000u), cg1 = __uint_as_float(cw1 & 0xFFFF0000u);
;     float csu0 = US[ci0], csu1 = US[ci1], csv0 = VS[ci0], csv1 = VS[ci1];
;     ...
;     EXP_XROW(t0);
;     u32x4 A[EB], B[EB];
; #pragma unroll
;     for (int e = 0; e < EB; ++e) A[e] = EXP_ROW(ci0, e);
; #pragma unroll
;     for (int e = 0; e < EB; ++e) B[e] = EXP_ROW(ci0, EB + e);
	v_min_u32_dpp v204, v230, v230 quad_perm:[1,0,3,2] row_mask:0xf bank_mask:0xf
	v_max_u32_dpp v205, v230, v230 quad_perm:[1,0,3,2] row_mask:0xf bank_mask:0xf
	v_cndmask_b32_e64 v229, v203, v202, s[58:59]
	v_cndmask_b32_e64 v230, v205, v204, s[58:59]
	s_nop 1
	v_permlane16_swap_b32_e32 v229, v230
	v_min_u32_e32 v202, v229, v230
	v_max_u32_e32 v230, v229, v230
	v_mov_b32_e32 v229, v202
	s_nop 1
	v_permlane32_swap_b32_e32 v229, v230
	v_min_u32_e32 v202, v229, v230
	v_max_u32_e32 v230, v229, v230
	v_mov_b32_e32 v229, v202
	s_nop 1
	v_permlane16_swap_b32_e32 v229, v230
	v_min_u32_e32 v202, v229, v230
	v_max_u32_e32 v230, v229, v230
	v_mov_b32_e32 v229, v202
	s_nop 1
	v_permlane16_swap_b32_e32 v229, v230
	s_nop 1
	v_permlane32_swap_b32_e32 v229, v230
	v_alignbit_b32 v229, v229, v229, 16
	v_alignbit_b32 v230, v230, v230, 16
	v_and_b32_e32 v231, 0x3fff, v229
	v_and_b32_e32 v232, 0x3fff, v230
	v_lshlrev_b32_e32 v2, 10, v231
	v_lshlrev_b32_e32 v3, 10, v232
	global_store_dword v192, v2, s[86:87]
	global_store_dword v192, v3, s[86:87] offset:256
	v_readlane_b32 s40, v231, 22
	v_readlane_b32 s41, v231, 23
	v_readlane_b32 s49, v231, 31
	v_lshlrev_b32_e32 v2, 2, v231
	v_lshlrev_b32_e32 v3, 2, v232
	v_add_u32_e32 v232, s94, v192
	v_readlane_b32 s33, v231, 15
	v_readlane_b32 s34, v231, 16
	v_readlane_b32 s35, v231, 17
	v_readlane_b32 s36, v231, 18
	v_readlane_b32 s37, v231, 19
	v_readlane_b32 s38, v231, 20
	v_readlane_b32 s39, v231, 21
	v_readlane_b32 s42, v231, 24
	v_readlane_b32 s43, v231, 25
	v_readlane_b32 s44, v231, 26
	v_readlane_b32 s45, v231, 27
	v_readlane_b32 s46, v231, 28
	v_readlane_b32 s47, v231, 29
	v_readlane_b32 s48, v231, 30
	v_lshl_or_b32 v42, s49, 10, v194
	v_lshl_or_b32 v50, s41, 10, v194
	v_lshl_or_b32 v51, s40, 10, v194
	v_readlane_b32 s30, v231, 13
	v_readlane_b32 s31, v231, 14
	global_load_dword v233, v2, s[12:13]
	global_load_dword v234, v3, s[12:13]
	global_load_dword v236, v3, s[14:15]
	global_load_dword v235, v2, s[14:15]
	v_lshl_or_b32 v43, s48, 10, v194
	v_lshl_or_b32 v44, s47, 10, v194
	v_lshl_or_b32 v45, s46, 10, v194
	v_lshl_or_b32 v46, s45, 10, v194
	v_lshl_or_b32 v47, s44, 10, v194
	v_lshl_or_b32 v48, s43, 10, v194
	v_lshl_or_b32 v49, s42, 10, v194
	global_load_dwordx4 v[2:5], v42, s[10:11]
	global_load_dwordx4 v[10:13], v43, s[10:11]
	global_load_dwordx4 v[6:9], v44, s[10:11]
	global_load_dwordx4 v[18:21], v45, s[10:11]
	global_load_dwordx4 v[14:17], v46, s[10:11]
	global_load_dwordx4 v[26:29], v47, s[10:11]
	global_load_dwordx4 v[22:25], v48, s[10:11]
	global_load_dwordx4 v[34:37], v49, s[10:11]
	global_load_dwordx4 v[30:33], v50, s[10:11]
	global_load_dwordx4 v[38:41], v51, s[10:11]
	v_lshl_or_b32 v50, s39, 10, v194
	v_lshl_or_b32 v51, s38, 10, v194
	v_lshl_or_b32 v58, s37, 10, v194
	v_lshl_or_b32 v59, s36, 10, v194
	v_lshl_or_b32 v66, s35, 10, v194
	v_lshl_or_b32 v67, s34, 10, v194
	v_lshl_or_b32 v75, s33, 10, v194
	v_readlane_b32 s28, v231, 11
	v_readlane_b32 s29, v231, 12
	global_load_dwordx4 v[42:45], v50, s[10:11]
	global_load_dwordx4 v[46:49], v51, s[10:11]
	s_nop 0
	global_load_dwordx4 v[50:53], v58, s[10:11]
	global_load_dwordx4 v[54:57], v59, s[10:11]
	s_nop 0
	global_load_dwordx4 v[58:61], v66, s[10:11]
	global_load_dwordx4 v[62:65], v67, s[10:11]
	v_lshl_or_b32 v76, s31, 10, v194
	global_load_dwordx4 v[66:69], v75, s[10:11]
	global_load_dwordx4 v[70:73], v76, s[10:11]
	v_lshl_or_b32 v75, s30, 10, v194
	v_readlane_b32 s25, v231, 9
	v_readlane_b32 s27, v231, 10
	v_lshl_or_b32 v76, s29, 10, v194
	global_load_dwordx4 v[112:115], v75, s[10:11]
	global_load_dwordx4 v[116:119], v76, s[10:11]
	v_lshl_or_b32 v75, s28, 10, v194
	v_readlane_b32 s23, v231, 7
	v_readlane_b32 s24, v231, 8
	v_lshl_or_b32 v76, s27, 10, v194
	global_load_dwordx4 v[144:147], v75, s[10:11]
	global_load_dwordx4 v[148:151], v76, s[10:11]
	v_lshl_or_b32 v75, s25, 10, v194
	v_readlane_b32 s21, v231, 5
	v_readlane_b32 s22, v231, 6
	v_lshl_or_b32 v76, s24, 10, v194
	global_load_dwordx4 v[152:155], v75, s[10:11]
	global_load_dwordx4 v[156:159], v76, s[10:11]
	v_lshl_or_b32 v75, s23, 10, v194
	v_readlane_b32 s19, v231, 3
	v_readlane_b32 s20, v231, 4
	v_lshl_or_b32 v76, s22, 10, v194
	global_load_dwordx4 v[160:163], v75, s[10:11]
	global_load_dwordx4 v[164:167], v76, s[10:11]
	v_lshl_or_b32 v75, s21, 10, v194
	v_readlane_b32 s16, v231, 1
	v_readlane_b32 s18, v231, 2
	v_lshl_or_b32 v76, s20, 10, v194
	global_load_dwordx4 v[168:171], v75, s[10:11]
	global_load_dwordx4 v[172:175], v76, s[10:11]
	v_lshl_or_b32 v75, s19, 10, v194
	v_readlane_b32 s9, v231, 0
	v_lshl_or_b32 v76, s18, 10, v194
	global_load_dwordx4 v[176:179], v75, s[10:11]
	global_load_dwordx4 v[180:183], v76, s[10:11]
	v_lshl_or_b32 v75, s16, 10, v194
	v_lshl_or_b32 v76, s9, 10, v194
	global_load_dwordx4 v[184:187], v75, s[10:11]
	global_load_dwordx4 v[188:191], v76, s[10:11]
	v_and_b32_e32 v75, 1, v0
	v_lshrrev_b32_e32 v76, 2, v0
	v_and_b32_e32 v0, 3, v0
	v_and_or_b32 v193, v76, 12, v0
	v_cmp_eq_u32_e64 s[2:3], 0, v75
	v_mbcnt_lo_u32_b32 v0, -1, 0
	s_mov_b32 s9, 0x800000
	s_mov_b32 s16, 0x45800000
	s_mov_b32 s27, 0x42ee0000
	s_mov_b32 s28, 0x3e6d3388
	s_mov_b32 s29, 0xc040c00
	s_mov_b32 s30, 0xc050c01
	s_mov_b32 s31, 0xc060c02
	s_mov_b32 s33, 0xc070c03
	v_mbcnt_hi_u32_b32 v228, -1, v0
	s_mov_b32 s20, s8
	s_branch .LBB0_1014
; __device__ __forceinline__ void expert_tokens(const unsigned char* __restrict__ UV, const float* __restrict__ US, const float* __restrict__ VS, ...
;     ...
;         float sy = 0.f;
;         const float sumc = wave_sum(sumc_l) * (0.25f / 4096.f);
; #pragma unroll
;         for (int i = 0; i < 16; ++i) { acc[i] = acc[i] * 4096.f - 7.5f * sumc; sy += acc[i] * acc[i]; }
.LBB0_1013:
	v_add_f32_dpp v66, v252, v252 quad_perm:[1,0,3,2] row_mask:0xf bank_mask:0xf bound_ctrl:1
	s_ashr_i32 s21, s20, 31
	s_lshl_b64 s[4:5], s[20:21], 12
	v_add_f32_dpp v66, v66, v66 quad_perm:[2,3,0,1] row_mask:0xf bank_mask:0xf bound_ctrl:1
	v_lshl_add_u64 v[162:163], v[200:201], 0, s[4:5]
	s_waitcnt vmcnt(31)
	v_mov_b64_e32 v[190:191], v[80:81]
	v_add_f32_dpp v66, v66, v66 row_ror:4 row_mask:0xf bank_mask:0xf bound_ctrl:1
	s_waitcnt vmcnt(30)
	v_mov_b64_e32 v[186:187], v[76:77]
	s_waitcnt vmcnt(29)
	v_mov_b64_e32 v[182:183], v[88:89]
	v_add_f32_dpp v66, v66, v66 row_ror:8 row_mask:0xf bank_mask:0xf bound_ctrl:1
	v_mov_b32_e32 v67, v66
	s_nop 1
	v_permlane16_swap_b32_e32 v66, v67
	v_add_f32_e32 v66, v66, v67
	v_mov_b32_e32 v67, v66
	s_nop 1
	v_permlane32_swap_b32_e32 v66, v67
	v_add_f32_e32 v66, v66, v67
	v_mul_f32_e32 v66, 0x38800000, v66
	v_mul_f32_e32 v66, 0x40f00000, v66
	v_pk_add_f32 v[224:225], v[224:225], v[220:221] neg_lo:[0,1] neg_hi:[0,1]
	v_pk_add_f32 v[222:223], v[222:223], v[218:219] neg_lo:[0,1] neg_hi:[0,1]
	v_pk_add_f32 v[216:217], v[216:217], v[212:213] neg_lo:[0,1] neg_hi:[0,1]
	v_pk_add_f32 v[214:215], v[214:215], v[210:211] neg_lo:[0,1] neg_hi:[0,1]
	s_mov_b32 s62, 0x43800000
	v_pk_fma_f32 v[118:119], v[224:225], s[16:17], v[66:67] op_sel_hi:[1,0,0] neg_lo:[0,0,1] neg_hi:[0,0,1]
	v_pk_fma_f32 v[144:145], v[222:223], s[16:17], v[66:67] op_sel_hi:[1,0,0] neg_lo:[0,0,1] neg_hi:[0,0,1]
	v_pk_mul_f32 v[68:69], v[118:119], v[118:119]
	v_pk_mul_f32 v[70:71], v[144:145], v[144:145]
	v_add_f32_e32 v68, v68, v69
	v_pk_fma_f32 v[148:149], v[220:221], s[62:63], v[66:67] op_sel_hi:[1,0,0] neg_lo:[0,0,1] neg_hi:[0,0,1]
	v_add_f32_e32 v68, v70, v68
	v_pk_mul_f32 v[72:73], v[148:149], v[148:149]
	v_add_f32_e32 v68, v71, v68
	v_pk_fma_f32 v[150:151], v[218:219], s[62:63], v[66:67] op_sel_hi:[1,0,0] neg_lo:[0,0,1] neg_hi:[0,0,1]
	v_add_f32_e32 v68, v72, v68
	v_pk_mul_f32 v[114:115], v[150:151], v[150:151]
	v_add_f32_e32 v68, v73, v68
	v_pk_fma_f32 v[152:153], v[216:217], s[16:17], v[66:67] op_sel_hi:[1,0,0] neg_lo:[0,0,1] neg_hi:[0,0,1]
	v_add_f32_e32 v68, v114, v68
	v_pk_mul_f32 v[116:117], v[152:153], v[152:153]
	v_add_f32_e32 v68, v115, v68
	v_pk_fma_f32 v[154:155], v[214:215], s[16:17], v[66:67] op_sel_hi:[1,0,0] neg_lo:[0,0,1] neg_hi:[0,0,1]
	v_add_f32_e32 v68, v116, v68
	v_pk_mul_f32 v[146:147], v[154:155], v[154:155]
	v_add_f32_e32 v68, v117, v68
	v_pk_fma_f32 v[156:157], v[212:213], s[62:63], v[66:67] op_sel_hi:[1,0,0] neg_lo:[0,0,1] neg_hi:[0,0,1]
	v_add_f32_e32 v68, v146, v68
	v_pk_mul_f32 v[158:159], v[156:157], v[156:157]
	v_add_f32_e32 v68, v147, v68
	v_pk_fma_f32 v[160:161], v[210:211], s[62:63], v[66:67] op_sel_hi:[1,0,0] neg_lo:[0,0,1] neg_hi:[0,0,1]
	v_add_f32_e32 v68, v158, v68
	v_pk_mul_f32 v[66:67], v[160:161], v[160:161]
	v_add_f32_e32 v68, v159, v68
	v_add_f32_e32 v66, v66, v68
	v_add_f32_e32 v66, v67, v66
	ds_read_b128 v[114:117], v240 offset:8192
	ds_read2st64_b64 v[70:73], v239 offset0:34 offset1:35
	v_add_f32_dpp v66, v66, v66 quad_perm:[1,0,3,2] row_mask:0xf bank_mask:0xf bound_ctrl:1
	s_waitcnt vmcnt(28)
	v_mov_b64_e32 v[178:179], v[84:85]
	s_waitcnt vmcnt(27)
	v_mov_b64_e32 v[174:175], v[96:97]
	v_add_f32_dpp v66, v66, v66 quad_perm:[2,3,0,1] row_mask:0xf bank_mask:0xf bound_ctrl:1
	s_waitcnt vmcnt(26)
; #define LAS __attribute__((address_space(3)))
; __device__ __forceinline__ void expert_tokens(const unsigned char* __restrict__ UV, const float* __restrict__ US, const float* __restrict__ VS, ...
;     ...
;         const float ry = rsqrtf(wave_sum(sy) * (1.f / 1024.f) + EPS);
;         const float pscale = (t < 2048) ? 1.f + pd : 1.f;
; #pragma unroll
;         for (int j = 0; j < 4; ++j) { const f32x4 y = (f32x4){acc[4 * j], acc[4 * j + 1], acc[4 * j + 2], acc[4 * j + 3]};
;             float* op = out + (size_t)t * 1024 + 256 * j + 4 * lane;
;             const u32x2 xw = *(const LAS u32x2*)(xrow + 512 * j + 8 * lane);
;             { const f32x4 ov_ = pscale * (f32x4){__uint_as_float(xw.x << 16), __uint_as_float(xw.x & 0xffff0000u), __uint_as_float(xw.y << 16), __uint_as_float(xw.y & 0xffff0000u)} + pscale * *(const LAS f32x4*)(pvt + 2048 + 256 * j + 4 * lane) * (y * ry); __builtin_nontemporal_store(ov_, (f32x4*)op); } }
;         ci0 = ni0; ci1 = ni1; cg0 = ng0; cg1 = ng1; csu0 = nsu0; csu1 = nsu1; csv0 = nsv0; csv1 = nsv1;
	v_mov_b64_e32 v[170:171], v[92:93]
	v_mov_b64_e32 v[188:189], v[78:79]
	v_add_f32_dpp v66, v66, v66 row_ror:4 row_mask:0xf bank_mask:0xf bound_ctrl:1
	v_mov_b64_e32 v[184:185], v[74:75]
	v_mov_b64_e32 v[180:181], v[86:87]
	v_add_f32_dpp v66, v66, v66 row_ror:8 row_mask:0xf bank_mask:0xf bound_ctrl:1
	v_mov_b32_e32 v67, v66
	s_nop 1
	v_permlane16_swap_b32_e32 v66, v67
	v_add_f32_e32 v66, v66, v67
	v_mov_b32_e32 v67, v66
	s_nop 1
	v_permlane32_swap_b32_e32 v66, v67
	v_add_f32_e32 v66, v66, v67
	v_fmamk_f32 v66, v66, 0x3a800000, v226
	v_mul_f32_e32 v67, 0x4b800000, v66
	v_cmp_gt_f32_e32 vcc, s9, v66
	v_mov_b64_e32 v[176:177], v[82:83]
	v_mov_b64_e32 v[172:173], v[94:95]
	v_cndmask_b32_e32 v66, v66, v67, vcc
	v_rsq_f32_e32 v66, v66
	v_mov_b64_e32 v[168:169], v[90:91]
	s_mov_b64 s[92:93], s[86:87]
	s_mov_b64 s[86:87], s[88:89]
	s_mov_b64 s[88:89], s[92:93]
	v_mul_f32_e32 v67, 0x45800000, v66
	v_cndmask_b32_e32 v158, v66, v67, vcc
	ds_read2st64_b64 v[66:69], v239 offset0:32 offset1:33
	v_pk_mul_f32 v[166:167], v[144:145], v[158:159] op_sel_hi:[1,0]
	ds_read_b128 v[144:147], v240 offset:9216
	v_pk_mul_f32 v[118:119], v[118:119], v[158:159] op_sel_hi:[1,0]
	s_and_b64 vcc, exec, s[18:19]
	s_waitcnt lgkmcnt(1)
	v_lshlrev_b32_e32 v164, 16, v66
	v_and_b32_e32 v165, 0xffff0000, v66
	v_lshlrev_b32_e32 v66, 16, v67
	v_and_b32_e32 v67, 0xffff0000, v67
	v_pk_fma_f32 v[116:117], v[116:117], v[166:167], v[66:67]
	v_pk_fma_f32 v[114:115], v[114:115], v[118:119], v[164:165]
	global_store_dwordx4 v[162:163], v[114:117], off nt
	v_lshlrev_b32_e32 v66, 16, v68
	v_and_b32_e32 v67, 0xffff0000, v68
	v_lshlrev_b32_e32 v68, 16, v69
	v_and_b32_e32 v69, 0xffff0000, v69
	v_pk_mul_f32 v[114:115], v[148:149], v[158:159] op_sel_hi:[1,0]
	v_pk_mul_f32 v[116:117], v[150:151], v[158:159] op_sel_hi:[1,0]
	s_waitcnt lgkmcnt(0)
	v_pk_fma_f32 v[66:67], v[144:145], v[114:115], v[66:67]
	v_pk_fma_f32 v[68:69], v[146:147], v[116:117], v[68:69]
	global_store_dwordx4 v[162:163], v[66:69], off offset:1024 nt
	ds_read_b128 v[66:69], v240 offset:10240
	ds_read_b128 v[114:117], v240 offset:11264
	v_lshlrev_b32_e32 v118, 16, v70
	v_and_b32_e32 v119, 0xffff0000, v70
	v_lshlrev_b32_e32 v70, 16, v71
	v_and_b32_e32 v71, 0xffff0000, v71
	v_pk_mul_f32 v[144:145], v[152:153], v[158:159] op_sel_hi:[1,0]
	v_pk_mul_f32 v[146:147], v[154:155], v[158:159] op_sel_hi:[1,0]
	s_waitcnt lgkmcnt(1)
	v_pk_fma_f32 v[66:67], v[66:67], v[144:145], v[118:119]
	v_pk_fma_f32 v[68:69], v[68:69], v[146:147], v[70:71]
	global_store_dwordx4 v[162:163], v[66:69], off offset:2048 nt
	v_pk_mul_f32 v[70:71], v[156:157], v[158:159] op_sel_hi:[1,0]
	s_waitcnt vmcnt(28)
	v_mov_b64_e32 v[166:167], v[104:105]
	v_lshlrev_b32_e32 v66, 16, v72
	v_and_b32_e32 v67, 0xffff0000, v72
	v_lshlrev_b32_e32 v68, 16, v73
	v_and_b32_e32 v69, 0xffff0000, v73
	v_pk_mul_f32 v[72:73], v[160:161], v[158:159] op_sel_hi:[1,0]
	s_waitcnt lgkmcnt(0)
	v_pk_fma_f32 v[66:67], v[114:115], v[70:71], v[66:67]
	v_pk_fma_f32 v[68:69], v[116:117], v[72:73], v[68:69]
	s_waitcnt vmcnt(26)
	v_mov_b64_e32 v[158:159], v[112:113]
	global_store_dwordx4 v[162:163], v[66:69], off offset:3072 nt
	v_mov_b64_e32 v[162:163], v[100:101]
	v_mov_b64_e32 v[156:157], v[110:111]
	s_waitcnt vmcnt(26)
	v_mov_b64_e32 v[154:155], v[108:109]
	s_waitcnt vmcnt(25)
	v_mov_b64_e32 v[150:151], v[126:127]
	s_waitcnt vmcnt(24)
	v_mov_b64_e32 v[146:147], v[122:123]
	s_waitcnt vmcnt(23)
	v_mov_b64_e32 v[116:117], v[132:133]
	s_waitcnt vmcnt(22)
	v_mov_b64_e32 v[112:113], v[128:129]
	s_waitcnt vmcnt(21)
	v_mov_b64_e32 v[70:71], v[140:141]
	s_waitcnt vmcnt(20)
	v_mov_b64_e32 v[66:67], v[136:137]
	v_mov_b64_e32 v[164:165], v[102:103]
	v_mov_b64_e32 v[160:161], v[98:99]
	v_mov_b64_e32 v[152:153], v[106:107]
	v_mov_b64_e32 v[148:149], v[124:125]
	v_mov_b64_e32 v[144:145], v[120:121]
	v_mov_b64_e32 v[118:119], v[134:135]
	v_mov_b64_e32 v[114:115], v[130:131]
	v_mov_b64_e32 v[72:73], v[142:143]
	v_mov_b64_e32 v[68:69], v[138:139]
	v_and_b32_e32 v229, 0xffff0000, v237
	ds_write_b32 v232, v229 offset:512
	v_and_b32_e32 v230, 0xffff0000, v238
	ds_write_b32 v232, v230 offset:768
	ds_write_b32 v232, v241
	ds_write_b32 v232, v0 offset:256
	v_mul_f32_e32 v235, s16, v245
	ds_write_b32 v232, v235 offset:1024
	v_mul_f32_e32 v236, s16, v246
	ds_write_b32 v232, v236 offset:1280
	s_mov_b32 s20, s34
	s_cbranch_vccnz .LBB0_1025

.Lp10_nobar_i:
	s_lshl_b32 s92, s21, 2
	s_cmp_lt_u32 s21, 0x80
	s_cselect_b32 s90, s86, s88
	s_cselect_b32 s91, s87, s89
	s_cselect_b32 s92, s92, 0
	s_add_u32 s90, s90, s92
	s_addc_u32 s91, s91, 0
	s_load_dwordx16 s[64:79], s[90:91], 0x0 glc
	v_dot8_i32_i4 v88, v248, v70, 0
	v_dot8_i32_i4 v88, v250, v71, v88
	s_nop 2
	v_lshlrev_b32_e32 v88, 4, v88
	v_dot8_i32_i4 v88, v247, v70, v88
	v_dot8_i32_i4 v74, v248, v188, 0
	v_dot8_i32_i4 v75, v248, v184, 0
	v_dot8_i32_i4 v76, v248, v180, 0
	v_dot8_i32_i4 v77, v248, v176, 0
	v_dot8_i32_i4 v78, v248, v172, 0
	v_dot8_i32_i4 v79, v248, v168, 0
	v_dot8_i32_i4 v80, v248, v164, 0
	v_dot8_i32_i4 v81, v248, v160, 0
	v_dot8_i32_i4 v82, v248, v156, 0
	v_dot8_i32_i4 v83, v248, v152, 0
	v_dot8_i32_i4 v84, v248, v148, 0
	v_dot8_i32_i4 v85, v248, v144, 0
	v_dot8_i32_i4 v86, v248, v116, 0
	v_dot8_i32_i4 v87, v248, v112, 0
	v_dot8_i32_i4 v70, v248, v66, 0
	v_dot8_i32_i4 v74, v250, v189, v74
	v_dot8_i32_i4 v75, v250, v185, v75
	v_dot8_i32_i4 v76, v250, v181, v76
	v_dot8_i32_i4 v77, v250, v177, v77
	v_dot8_i32_i4 v78, v250, v173, v78
	v_dot8_i32_i4 v79, v250, v169, v79
	v_dot8_i32_i4 v80, v250, v165, v80
	v_dot8_i32_i4 v81, v250, v161, v81
	v_dot8_i32_i4 v82, v250, v157, v82
	v_dot8_i32_i4 v83, v250, v153, v83
	v_dot8_i32_i4 v84, v250, v149, v84
	v_dot8_i32_i4 v85, v250, v145, v85
	v_dot8_i32_i4 v86, v250, v117, v86
	v_dot8_i32_i4 v87, v250, v113, v87
	v_dot8_i32_i4 v70, v250, v67, v70
	v_lshlrev_b32_e32 v74, 4, v74
	v_lshlrev_b32_e32 v75, 4, v75
	v_lshlrev_b32_e32 v76, 4, v76
	v_lshlrev_b32_e32 v77, 4, v77
	v_lshlrev_b32_e32 v78, 4, v78
	v_lshlrev_b32_e32 v79, 4, v79
	v_lshlrev_b32_e32 v80, 4, v80
	v_lshlrev_b32_e32 v81, 4, v81
	v_lshlrev_b32_e32 v82, 4, v82
	v_lshlrev_b32_e32 v83, 4, v83
	v_lshlrev_b32_e32 v84, 4, v84
	v_lshlrev_b32_e32 v85, 4, v85
	v_lshlrev_b32_e32 v86, 4, v86
	v_lshlrev_b32_e32 v87, 4, v87
	v_lshlrev_b32_e32 v70, 4, v70
	v_dot8_i32_i4 v74, v247, v188, v74
	v_dot8_i32_i4 v75, v247, v184, v75
	v_dot8_i32_i4 v76, v247, v180, v76
	v_dot8_i32_i4 v77, v247, v176, v77
	v_dot8_i32_i4 v78, v247, v172, v78
	v_dot8_i32_i4 v79, v247, v168, v79
	v_dot8_i32_i4 v80, v247, v164, v80
	v_dot8_i32_i4 v81, v247, v160, v81
	v_dot8_i32_i4 v82, v247, v156, v82
	v_dot8_i32_i4 v83, v247, v152, v83
	v_dot8_i32_i4 v84, v247, v148, v84
	v_dot8_i32_i4 v85, v247, v144, v85
	v_dot8_i32_i4 v86, v247, v116, v86
	v_dot8_i32_i4 v87, v247, v112, v87
	v_dot8_i32_i4 v70, v247, v66, v70
	v_dot8_i32_i4 v74, v249, v189, v74
	v_dot8_i32_i4 v75, v249, v185, v75
	v_dot8_i32_i4 v76, v249, v181, v76
	v_dot8_i32_i4 v77, v249, v177, v77
	v_dot8_i32_i4 v78, v249, v173, v78
	v_dot8_i32_i4 v79, v249, v169, v79
	v_dot8_i32_i4 v80, v249, v165, v80
	v_dot8_i32_i4 v81, v249, v161, v81
	v_dot8_i32_i4 v82, v249, v157, v82
	v_dot8_i32_i4 v83, v249, v153, v83
	v_dot8_i32_i4 v84, v249, v149, v84
	v_dot8_i32_i4 v85, v249, v145, v85
	v_dot8_i32_i4 v86, v249, v117, v86
	v_dot8_i32_i4 v87, v249, v113, v87
	v_dot8_i32_i4 v88, v249, v71, v88
	v_dot8_i32_i4 v70, v249, v67, v70
	v_permlane32_swap_b32_e32 v74, v82
	v_permlane32_swap_b32_e32 v75, v83
	v_permlane32_swap_b32_e32 v76, v84
	v_permlane32_swap_b32_e32 v77, v85
	v_permlane32_swap_b32_e32 v78, v86
	v_permlane32_swap_b32_e32 v79, v87
	v_permlane32_swap_b32_e32 v80, v88
	v_permlane32_swap_b32_e32 v81, v70
	v_add_u32_e32 v66, v74, v82
	v_add_u32_e32 v67, v75, v83
	v_add_u32_e32 v71, v76, v84
	v_add_u32_e32 v74, v77, v85
	v_add_u32_e32 v75, v78, v86
	v_add_u32_e32 v76, v79, v87
	v_add_u32_e32 v77, v80, v88
	v_add_u32_e32 v70, v81, v70
	v_permlane16_swap_b32_e32 v66, v75
	v_permlane16_swap_b32_e32 v67, v76
	v_permlane16_swap_b32_e32 v71, v77
	v_permlane16_swap_b32_e32 v74, v70
	v_add_u32_e32 v66, v66, v75
	v_add_u32_e32 v67, v67, v76
	v_add_u32_e32 v71, v71, v77
	v_add_u32_e32 v70, v74, v70
	v_cndmask_b32_e64 v74, v71, v66, s[0:1]
	v_cndmask_b32_e64 v66, v66, v71, s[0:1]
	v_cndmask_b32_e64 v71, v70, v67, s[0:1]
	v_cndmask_b32_e64 v67, v67, v70, s[0:1]
	v_add_u32_dpp v66, v66, v74 quad_perm:[2,3,0,1] row_mask:0xf bank_mask:0xf bound_ctrl:1
	s_sub_i32 s4, s21, 32
	s_lshl_b32 s93, s4, 2
	s_add_i32 s93, s93, s94
	v_add_u32_dpp v67, v67, v71 quad_perm:[2,3,0,1] row_mask:0xf bank_mask:0xf bound_ctrl:1
	v_cndmask_b32_e64 v70, v67, v66, s[2:3]
	v_cndmask_b32_e64 v66, v66, v67, s[2:3]
	s_cmp_lt_u32 s25, 4
	s_cselect_b64 vcc, -1, 0
	v_add_u32_dpp v66, v66, v70 quad_perm:[1,0,3,2] row_mask:0xf bank_mask:0xf bound_ctrl:1
	s_nop 1
	v_add_u32_dpp v66, v66, v66 row_ror:8 row_mask:0xf bank_mask:0xf bound_ctrl:1
	s_cmp_eq_u32 s21, 32
	s_nop 0
	v_add_u32_dpp v67, v66, v66 row_ror:4 row_mask:0xf bank_mask:0xf bound_ctrl:1
	v_lshl_add_u32 v66, v193, 2, s93
	v_cvt_f32_i32_e32 v74, v67
	s_waitcnt lgkmcnt(0)
	ds_read_b32 v75, v66
	ds_read_b32 v76, v66 offset:512
	v_add_f32_e32 v71, v251, v74
	v_mul_f32_e32 v71, v244, v71
	s_waitcnt lgkmcnt(1)
	v_mul_f32_e32 v74, v71, v75
	v_fma_f32 v71, |v74|, s28, 1.0
	v_rcp_f32_e32 v75, v71
	v_mul_f32_e32 v79, v74, v74
	v_mul_f32_e32 v79, 0xbf38aa3b, v79
	v_exp_f32_e32 v79, v79
	v_fmamk_f32 v78, v75, 0x3f07dc22, v227
	v_fmaak_f32 v78, v75, v78, 0x3f35f0e3
	v_fmaak_f32 v78, v75, v78, 0xbe11a98e
	v_fmaak_f32 v78, v75, v78, 0x3e027906
	ds_read_b32 v77, v66 offset:1024
	v_mul_f32_e32 v75, v75, v78
	v_mul_f32_e32 v75, v79, v75
	v_mul_f32_e32 v78, v74, v75
	v_fma_f32 v75, -v74, v75, v74
	v_cmp_gt_f32_e32 vcc, 0, v74
	s_nop 1
	v_cndmask_b32_e32 v74, v75, v78, vcc
	s_waitcnt lgkmcnt(1)
	v_mul_f32_e32 v74, v74, v76
	s_cselect_b64 vcc, -1, 0
	s_cmp_gt_u32 s25, 5
	s_waitcnt lgkmcnt(0)
	v_mul_f32_e32 v74, v74, v77
	s_cselect_b64 s[22:23], -1, 0
	s_cmp_lt_u32 s25, 6
	s_cselect_b64 s[4:5], -1, 0
	s_nop 1
	v_mov_b32_dpp v207, v74 quad_perm:[1,0,3,2] row_mask:0xf bank_mask:0xf
	s_cmp_lg_u32 s21, 32
	v_cvt_pk_f16_f32 v209, v74, v207
	v_cvt_f32_f16_e32 v116, v209
	s_nop 0
	v_readlane_b32 s47, v209, 0
	v_readlane_b32 s45, v209, 2
	v_readlane_b32 s43, v209, 16
	v_readlane_b32 s41, v209, 18
	v_readlane_b32 s39, v209, 32
	v_readlane_b32 s37, v209, 34
	v_readlane_b32 s35, v209, 48
	v_readlane_b32 s4, v209, 50
	buffer_load_dwordx4 v[78:81], v194, s[80:83], s64 offen
	buffer_load_dwordx4 v[74:77], v194, s[80:83], s65 offen
	buffer_load_dwordx4 v[86:89], v194, s[80:83], s66 offen
	buffer_load_dwordx4 v[82:85], v194, s[80:83], s67 offen
	buffer_load_dwordx4 v[94:97], v194, s[80:83], s68 offen
	buffer_load_dwordx4 v[90:93], v194, s[80:83], s69 offen
	buffer_load_dwordx4 v[102:105], v194, s[80:83], s70 offen
	buffer_load_dwordx4 v[98:101], v194, s[80:83], s71 offen
	buffer_load_dwordx4 v[110:113], v194, s[80:83], s72 offen
	buffer_load_dwordx4 v[106:109], v194, s[80:83], s73 offen
	buffer_load_dwordx4 v[124:127], v194, s[80:83], s74 offen
	buffer_load_dwordx4 v[120:123], v194, s[80:83], s75 offen
	buffer_load_dwordx4 v[132:135], v194, s[80:83], s76 offen
	buffer_load_dwordx4 v[128:131], v194, s[80:83], s77 offen
	buffer_load_dwordx4 v[140:143], v194, s[80:83], s78 offen
	buffer_load_dwordx4 v[136:139], v194, s[80:83], s79 offen
	s_cbranch_scc1 .LBB0_1021
; __device__ __forceinline__ void expert_tokens(const unsigned char* __restrict__ UV, const float* __restrict__ US, const float* __restrict__ VS, ...
;     ...
;         const unsigned nw0 = (unsigned)IDX[(size_t)tn * 128 + lane], nw1 = (unsigned)IDX[(size_t)tn * 128 + 64 + lane];
;         const int ni0 = (int)nw0 & rmask, ni1 = (int)nw1 & rmask;
;         const float ng0 = __uint_as_float(nw0 & 0xFFFF0000u), ng1 = __uint_as_float(nw1 & 0xFFFF0000u);
	s_waitcnt vmcnt(16)
	s_bfe_i32 s60, s34, 0x10000
	v_alignbit_b32 v237, v237, v237, 16
	v_alignbit_b32 v238, v238, v238, 16
	v_xor_b32_e32 v237, s60, v237
	v_xor_b32_e32 v238, s60, v238
	s_nop 1
	s_mov_b32 s58, 0x99999999
	s_mov_b32 s59, 0x99999999
	v_min_u32_dpp v202, v237, v237 quad_perm:[1,0,3,2] row_mask:0xf bank_mask:0xf
	v_max_u32_dpp v203, v237, v237 quad_perm:[1,0,3,2] row_mask:0xf bank_mask:0xf
	v_min_u32_dpp v204, v238, v238 quad_perm:[1,0,3,2] row_mask:0xf bank_mask:0xf
	v_max_u32_dpp v205, v238, v238 quad_perm:[1,0,3,2] row_mask:0xf bank_mask:0xf
	v_cndmask_b32_e64 v237, v203, v202, s[58:59]
	v_cndmask_b32_e64 v238, v205, v204, s[58:59]
	s_mov_b32 s58, 0xcc33cc33
	s_mov_b32 s59, 0xcc33cc33
	v_min_u32_dpp v202, v237, v237 quad_perm:[2,3,0,1] row_mask:0xf bank_mask:0xf
	v_max_u32_dpp v203, v237, v237 quad_perm:[2,3,0,1] row_mask:0xf bank_mask:0xf
	v_min_u32_dpp v204, v238, v238 quad_perm:[2,3,0,1] row_mask:0xf bank_mask:0xf
	v_max_u32_dpp v205, v238, v238 quad_perm:[2,3,0,1] row_mask:0xf bank_mask:0xf
	v_cndmask_b32_e64 v237, v203, v202, s[58:59]
	v_cndmask_b32_e64 v238, v205, v204, s[58:59]
	s_mov_b32 s58, 0xaa55aa55
	s_mov_b32 s59, 0xaa55aa55
	v_min_u32_dpp v202, v237, v237 quad_perm:[1,0,3,2] row_mask:0xf bank_mask:0xf
	v_max_u32_dpp v203, v237, v237 quad_perm:[1,0,3,2] row_mask:0xf bank_mask:0xf
	v_min_u32_dpp v204, v238, v238 quad_perm:[1,0,3,2] row_mask:0xf bank_mask:0xf
	v_max_u32_dpp v205, v238, v238 quad_perm:[1,0,3,2] row_mask:0xf bank_mask:0xf
	v_cndmask_b32_e64 v237, v203, v202, s[58:59]
	v_cndmask_b32_e64 v238, v205, v204, s[58:59]
	s_mov_b32 s58, 0xf00ff00f
	s_mov_b32 s59, 0xf00ff00f
	v_min_u32_dpp v202, v237, v237 row_ror:8 row_mask:0xf bank_mask:0xf
	v_max_u32_dpp v203, v237, v237 row_ror:8 row_mask:0xf bank_mask:0xf
	v_min_u32_dpp v204, v238, v238 row_ror:8 row_mask:0xf bank_mask:0xf
	v_max_u32_dpp v205, v238, v238 row_ror:8 row_mask:0xf bank_mask:0xf
	v_cndmask_b32_e64 v237, v203, v202, s[58:59]
	v_cndmask_b32_e64 v238, v205, v204, s[58:59]
	s_mov_b32 s58, 0xc3c3c3c3
	s_mov_b32 s59, 0xc3c3c3c3
	v_min_u32_dpp v202, v237, v237 quad_perm:[2,3,0,1] row_mask:0xf bank_mask:0xf
	v_max_u32_dpp v203, v237, v237 quad_perm:[2,3,0,1] row_mask:0xf bank_mask:0xf
	v_min_u32_dpp v204, v238, v238 quad_perm:[2,3,0,1] row_mask:0xf bank_mask:0xf
	v_max_u32_dpp v205, v238, v238 quad_perm:[2,3,0,1] row_mask:0xf bank_mask:0xf
	v_cndmask_b32_e64 v237, v203, v202, s[58:59]
	v_cndmask_b32_e64 v238, v205, v204, s[58:59]
	s_mov_b32 s58, 0xa5a5a5a5
	s_mov_b32 s59, 0xa5a5a5a5
	v_min_u32_dpp v202, v237, v237 quad_perm:[1,0,3,2] row_mask:0xf bank_mask:0xf
	v_max_u32_dpp v203, v237, v237 quad_perm:[1,0,3,2] row_mask:0xf bank_mask:0xf
	v_min_u32_dpp v204, v238, v238 quad_perm:[1,0,3,2] row_mask:0xf bank_mask:0xf
	v_max_u32_dpp v205, v238, v238 quad_perm:[1,0,3,2] row_mask:0xf bank_mask:0xf
	v_cndmask_b32_e64 v237, v203, v202, s[58:59]
	v_cndmask_b32_e64 v238, v205, v204, s[58:59]
	s_mov_b32 s58, 0xf0f00f0f
	s_mov_b32 s59, 0xf0f00f0f
	v_mov_b32_dpp v202, v237 row_half_mirror row_mask:0xf bank_mask:0xf
	v_mov_b32_dpp v204, v238 row_half_mirror row_mask:0xf bank_mask:0xf
	s_nop 0
	v_max_u32_dpp v203, v202, v237 quad_perm:[3,2,1,0] row_mask:0xf bank_mask:0xf
	v_max_u32_dpp v205, v204, v238 quad_perm:[3,2,1,0] row_mask:0xf bank_mask:0xf
	v_min_u32_dpp v202, v202, v237 quad_perm:[3,2,1,0] row_mask:0xf bank_mask:0xf
	v_min_u32_dpp v204, v204, v238 quad_perm:[3,2,1,0] row_mask:0xf bank_mask:0xf
	v_cndmask_b32_e64 v237, v203, v202, s[58:59]
	v_cndmask_b32_e64 v238, v205, v204, s[58:59]
	s_mov_b32 s58, 0xff0000ff
	s_mov_b32 s59, 0xff0000ff
	v_min_u32_dpp v202, v237, v237 row_ror:8 row_mask:0xf bank_mask:0xf
	v_max_u32_dpp v203, v237, v237 row_ror:8 row_mask:0xf bank_mask:0xf
	v_min_u32_dpp v204, v238, v238 row_ror:8 row_mask:0xf bank_mask:0xf
	v_max_u32_dpp v205, v238, v238 row_ror:8 row_mask:0xf bank_mask:0xf
	v_cndmask_b32_e64 v237, v203, v202, s[58:59]
	v_cndmask_b32_e64 v238, v205, v204, s[58:59]
	s_mov_b32 s58, 0xcccc3333
	s_mov_b32 s59, 0xcccc3333
	v_min_u32_dpp v202, v237, v237 quad_perm:[2,3,0,1] row_mask:0xf bank_mask:0xf
	v_max_u32_dpp v203, v237, v237 quad_perm:[2,3,0,1] row_mask:0xf bank_mask:0xf
	v_min_u32_dpp v204, v238, v238 quad_perm:[2,3,0,1] row_mask:0xf bank_mask:0xf
	v_max_u32_dpp v205, v238, v238 quad_perm:[2,3,0,1] row_mask:0xf bank_mask:0xf
	v_cndmask_b32_e64 v237, v203, v202, s[58:59]
	v_cndmask_b32_e64 v238, v205, v204, s[58:59]
	s_mov_b32 s58, 0xaaaa5555
	s_mov_b32 s59, 0xaaaa5555
	v_min_u32_dpp v202, v237, v237 quad_perm:[1,0,3,2] row_mask:0xf bank_mask:0xf
	v_max_u32_dpp v203, v237, v237 quad_perm:[1,0,3,2] row_mask:0xf bank_mask:0xf
	v_min_u32_dpp v204, v238, v238 quad_perm:[1,0,3,2] row_mask:0xf bank_mask:0xf
	v_max_u32_dpp v205, v238, v238 quad_perm:[1,0,3,2] row_mask:0xf bank_mask:0xf
	v_cndmask_b32_e64 v237, v203, v202, s[58:59]
	v_cndmask_b32_e64 v238, v205, v204, s[58:59]
	s_nop 1
	v_permlane16_swap_b32_e32 v237, v238
	s_mov_b32 s58, -1
	s_mov_b32 s59, 0
	v_min_u32_e32 v202, v237, v238
	v_max_u32_e32 v203, v237, v238
	v_cndmask_b32_e64 v237, v203, v202, s[58:59]
	v_cndmask_b32_e64 v238, v202, v203, s[58:59]
	s_mov_b32 s58, 0xf0f0f0f
	s_mov_b32 s59, 0xf0f0f0f0
	v_mov_b32_dpp v202, v237 row_half_mirror row_mask:0xf bank_mask:0xf
	v_mov_b32_dpp v204, v238 row_half_mirror row_mask:0xf bank_mask:0xf
	s_nop 0
	v_max_u32_dpp v203, v202, v237 quad_perm:[3,2,1,0] row_mask:0xf bank_mask:0xf
	v_max_u32_dpp v205, v204, v238 quad_perm:[3,2,1,0] row_mask:0xf bank_mask:0xf
	v_min_u32_dpp v202, v202, v237 quad_perm:[3,2,1,0] row_mask:0xf bank_mask:0xf
	v_min_u32_dpp v204, v204, v238 quad_perm:[3,2,1,0] row_mask:0xf bank_mask:0xf
; __device__ __forceinline__ void expert_tokens(const unsigned char* __restrict__ UV, const float* __restrict__ US, const float* __restrict__ VS, ...
;     ...
;         const unsigned nw0 = (unsigned)IDX[(size_t)tn * 128 + lane], nw1 = (unsigned)IDX[(size_t)tn * 128 + 64 + lane];
;         const int ni0 = (int)nw0 & rmask, ni1 = (int)nw1 & rmask;
;         const float ng0 = __uint_as_float(nw0 & 0xFFFF0000u), ng1 = __uint_as_float(nw1 & 0xFFFF0000u);
;     ...
;             if (bi == 0) { nsu0 = US[ni0]; nsu1 = US[ni1]; nsv0 = VS[ni0]; nsv1 = VS[ni1]; }
	v_cndmask_b32_e64 v237, v203, v202, s[58:59]
	v_cndmask_b32_e64 v238, v205, v204, s[58:59]
	s_mov_b32 s58, 0xff00ff
	s_mov_b32 s59, 0xff00ff00
	v_min_u32_dpp v202, v237, v237 row_ror:8 row_mask:0xf bank_mask:0xf
	v_max_u32_dpp v203, v237, v237 row_ror:8 row_mask:0xf bank_mask:0xf
	v_min_u32_dpp v204, v238, v238 row_ror:8 row_mask:0xf bank_mask:0xf
	v_max_u32_dpp v205, v238, v238 row_ror:8 row_mask:0xf bank_mask:0xf
	v_cndmask_b32_e64 v237, v203, v202, s[58:59]
	v_cndmask_b32_e64 v238, v205, v204, s[58:59]
	s_mov_b32 s58, 0x33333333
	s_mov_b32 s59, 0xcccccccc
	v_min_u32_dpp v202, v237, v237 quad_perm:[2,3,0,1] row_mask:0xf bank_mask:0xf
	v_max_u32_dpp v203, v237, v237 quad_perm:[2,3,0,1] row_mask:0xf bank_mask:0xf
	v_min_u32_dpp v204, v238, v238 quad_perm:[2,3,0,1] row_mask:0xf bank_mask:0xf
	v_max_u32_dpp v205, v238, v238 quad_perm:[2,3,0,1] row_mask:0xf bank_mask:0xf
	v_cndmask_b32_e64 v237, v203, v202, s[58:59]
	v_cndmask_b32_e64 v238, v205, v204, s[58:59]
	s_mov_b32 s58, 0x55555555
	s_mov_b32 s59, 0xaaaaaaaa
	v_min_u32_dpp v202, v237, v237 quad_perm:[1,0,3,2] row_mask:0xf bank_mask:0xf
	v_max_u32_dpp v203, v237, v237 quad_perm:[1,0,3,2] row_mask:0xf bank_mask:0xf
	v_min_u32_dpp v204, v238, v238 quad_perm:[1,0,3,2] row_mask:0xf bank_mask:0xf
	v_max_u32_dpp v205, v238, v238 quad_perm:[1,0,3,2] row_mask:0xf bank_mask:0xf
	v_cndmask_b32_e64 v237, v203, v202, s[58:59]
	v_cndmask_b32_e64 v238, v205, v204, s[58:59]
	s_nop 1
	v_permlane32_swap_b32_e32 v237, v238
	s_mov_b32 s58, 0xffff
	s_mov_b32 s59, 0xffff
	v_min_u32_e32 v202, v237, v238
	v_max_u32_e32 v203, v237, v238
	v_cndmask_b32_e64 v237, v203, v202, s[58:59]
	v_cndmask_b32_e64 v238, v202, v203, s[58:59]
	s_nop 1
	v_permlane32_swap_b32_e32 v237, v238
	s_mov_b32 s58, 0xffff
	s_mov_b32 s59, 0xffff
	v_min_u32_e32 v202, v237, v238
	v_max_u32_e32 v203, v237, v238
	v_cndmask_b32_e64 v237, v203, v202, s[58:59]
	v_cndmask_b32_e64 v238, v202, v203, s[58:59]
	s_mov_b32 s58, 0xf0f00f0f
	s_mov_b32 s59, 0xf0f00f0f
	v_mov_b32_dpp v202, v237 row_half_mirror row_mask:0xf bank_mask:0xf
	v_mov_b32_dpp v204, v238 row_half_mirror row_mask:0xf bank_mask:0xf
	s_nop 0
	v_max_u32_dpp v203, v202, v237 quad_perm:[3,2,1,0] row_mask:0xf bank_mask:0xf
	v_max_u32_dpp v205, v204, v238 quad_perm:[3,2,1,0] row_mask:0xf bank_mask:0xf
	v_min_u32_dpp v202, v202, v237 quad_perm:[3,2,1,0] row_mask:0xf bank_mask:0xf
	v_min_u32_dpp v204, v204, v238 quad_perm:[3,2,1,0] row_mask:0xf bank_mask:0xf
	v_cndmask_b32_e64 v237, v203, v202, s[58:59]
	v_cndmask_b32_e64 v238, v205, v204, s[58:59]
	s_mov_b32 s58, 0xff0000ff
	s_mov_b32 s59, 0xff0000ff
	v_min_u32_dpp v202, v237, v237 row_ror:8 row_mask:0xf bank_mask:0xf
	v_max_u32_dpp v203, v237, v237 row_ror:8 row_mask:0xf bank_mask:0xf
	v_min_u32_dpp v204, v238, v238 row_ror:8 row_mask:0xf bank_mask:0xf
	v_max_u32_dpp v205, v238, v238 row_ror:8 row_mask:0xf bank_mask:0xf
	v_cndmask_b32_e64 v237, v203, v202, s[58:59]
	v_cndmask_b32_e64 v238, v205, v204, s[58:59]
	s_mov_b32 s58, 0xcccc3333
	s_mov_b32 s59, 0xcccc3333
	v_min_u32_dpp v202, v237, v237 quad_perm:[2,3,0,1] row_mask:0xf bank_mask:0xf
	v_max_u32_dpp v203, v237, v237 quad_perm:[2,3,0,1] row_mask:0xf bank_mask:0xf
	v_min_u32_dpp v204, v238, v238 quad_perm:[2,3,0,1] row_mask:0xf bank_mask:0xf
	v_max_u32_dpp v205, v238, v238 quad_perm:[2,3,0,1] row_mask:0xf bank_mask:0xf
	v_cndmask_b32_e64 v237, v203, v202, s[58:59]
	v_cndmask_b32_e64 v238, v205, v204, s[58:59]
	s_mov_b32 s58, 0xaaaa5555
	s_mov_b32 s59, 0xaaaa5555
	v_min_u32_dpp v202, v237, v237 quad_perm:[1,0,3,2] row_mask:0xf bank_mask:0xf
	v_max_u32_dpp v203, v237, v237 quad_perm:[1,0,3,2] row_mask:0xf bank_mask:0xf
	v_min_u32_dpp v204, v238, v238 quad_perm:[1,0,3,2] row_mask:0xf bank_mask:0xf
	v_max_u32_dpp v205, v238, v238 quad_perm:[1,0,3,2] row_mask:0xf bank_mask:0xf
	v_cndmask_b32_e64 v237, v203, v202, s[58:59]
	v_cndmask_b32_e64 v238, v205, v204, s[58:59]
	s_nop 1
	v_permlane16_swap_b32_e32 v237, v238
	v_min_u32_e32 v202, v237, v238
	v_max_u32_e32 v238, v237, v238
	v_mov_b32_e32 v237, v202
	s_nop 1
	v_permlane32_swap_b32_e32 v237, v238
	v_min_u32_e32 v202, v237, v238
	v_max_u32_e32 v238, v237, v238
	v_mov_b32_e32 v237, v202
	s_nop 1
	v_permlane16_swap_b32_e32 v237, v238
	v_min_u32_e32 v202, v237, v238
	v_max_u32_e32 v238, v237, v238
	v_mov_b32_e32 v237, v202
	s_nop 1
	v_permlane16_swap_b32_e32 v237, v238
	s_nop 1
	v_permlane32_swap_b32_e32 v237, v238
	v_xor_b32_e32 v237, s60, v237
	v_xor_b32_e32 v238, s60, v238
	v_alignbit_b32 v237, v237, v237, 16
	v_alignbit_b32 v238, v238, v238, 16
	v_and_b32_e32 v242, 0x3fff, v237
	v_and_b32_e32 v243, 0x3fff, v238
	v_lshlrev_b32_e32 v208, 2, v242
	v_lshlrev_b32_e32 v206, 2, v243
	v_lshlrev_b32_e32 v204, 10, v242
	v_lshlrev_b32_e32 v205, 10, v243
	global_store_dword v192, v204, s[88:89]
	global_store_dword v192, v205, s[88:89] offset:256
	global_load_dword v241, v208, s[12:13]
	global_load_dword v0, v206, s[12:13]
	global_load_dword v245, v208, s[14:15]
	global_load_dword v246, v206, s[14:15]
.LBB0_1021:
	s_lshl_b32 s92, s21, 2
	s_cmp_lt_u32 s21, 0x80
	s_cselect_b32 s90, s86, s88
	s_cselect_b32 s91, s87, s89
	s_cselect_b32 s92, s92, 0
	s_add_u32 s90, s90, s92
	s_addc_u32 s91, s91, 0
	s_load_dwordx16 s[64:79], s[90:91], 0x40 glc
	v_perm_b32 v149, v186, v190, s29
	v_dot2c_f32_f16_e32 v224, s47, v149
	v_and_b32_e32 v149, s32, v149
	v_dot2c_f32_f16_e32 v220, s47, v149
	v_perm_b32 v149, v186, v190, s30
	v_dot2c_f32_f16_e32 v225, s47, v149
	v_and_b32_e32 v149, s32, v149
	v_dot2c_f32_f16_e32 v221, s47, v149
	v_perm_b32 v149, v186, v190, s31
	v_perm_b32 v117, v186, v190, s33
	v_dot2c_f32_f16_e32 v223, s47, v117
	v_and_b32_e32 v117, s32, v117
	v_dot2c_f32_f16_e32 v222, s47, v149
	v_and_b32_e32 v149, s32, v149
	v_dot2c_f32_f16_e32 v219, s47, v117
	v_dot2c_f32_f16_e32 v218, s47, v149
	v_perm_b32 v149, v187, v191, s29
	v_dot2c_f32_f16_e32 v216, s47, v149
	v_and_b32_e32 v149, s32, v149
	v_dot2c_f32_f16_e32 v212, s47, v149
	v_perm_b32 v149, v187, v191, s30
	v_dot2c_f32_f16_e32 v217, s47, v149
	v_and_b32_e32 v149, s32, v149
	v_dot2c_f32_f16_e32 v213, s47, v149
	v_perm_b32 v149, v187, v191, s31
	v_perm_b32 v117, v187, v191, s33
	v_dot2c_f32_f16_e32 v215, s47, v117
	v_and_b32_e32 v117, s32, v117
	v_dot2c_f32_f16_e32 v214, s47, v149
	v_and_b32_e32 v149, s32, v149
	v_dot2c_f32_f16_e32 v211, s47, v117
	v_dot2c_f32_f16_e32 v210, s47, v149
	v_perm_b32 v149, v178, v182, s29
	v_dot2c_f32_f16_e32 v224, s45, v149
	v_and_b32_e32 v149, s32, v149
	v_dot2c_f32_f16_e32 v220, s45, v149
	v_perm_b32 v149, v178, v182, s30
	v_dot2c_f32_f16_e32 v225, s45, v149
	v_and_b32_e32 v149, s32, v149
	v_dot2c_f32_f16_e32 v221, s45, v149
	v_perm_b32 v149, v178, v182, s31
	v_perm_b32 v117, v178, v182, s33
	v_dot2c_f32_f16_e32 v223, s45, v117
	v_and_b32_e32 v117, s32, v117
	v_dot2c_f32_f16_e32 v222, s45, v149
	v_and_b32_e32 v149, s32, v149
	v_dot2c_f32_f16_e32 v219, s45, v117
	v_dot2c_f32_f16_e32 v218, s45, v149
	v_perm_b32 v149, v179, v183, s29
	v_dot2c_f32_f16_e32 v216, s45, v149
	v_and_b32_e32 v149, s32, v149
	v_dot2c_f32_f16_e32 v212, s45, v149
	v_perm_b32 v149, v179, v183, s30
	v_dot2c_f32_f16_e32 v217, s45, v149
	v_and_b32_e32 v149, s32, v149
	v_dot2c_f32_f16_e32 v213, s45, v149
	v_perm_b32 v149, v179, v183, s31
	v_perm_b32 v117, v179, v183, s33
	v_dot2c_f32_f16_e32 v215, s45, v117
	v_and_b32_e32 v117, s32, v117
	v_dot2c_f32_f16_e32 v214, s45, v149
	v_and_b32_e32 v149, s32, v149
	v_dot2c_f32_f16_e32 v211, s45, v117
	v_dot2c_f32_f16_e32 v210, s45, v149
	v_perm_b32 v149, v170, v174, s29
	v_dot2c_f32_f16_e32 v224, s43, v149
	v_and_b32_e32 v149, s32, v149
	v_dot2c_f32_f16_e32 v220, s43, v149
	v_perm_b32 v149, v170, v174, s30
	v_dot2c_f32_f16_e32 v225, s43, v149
	v_and_b32_e32 v149, s32, v149
	v_dot2c_f32_f16_e32 v221, s43, v149
	v_perm_b32 v149, v170, v174, s31
	v_perm_b32 v117, v170, v174, s33
	v_dot2c_f32_f16_e32 v223, s43, v117
	v_and_b32_e32 v117, s32, v117
	v_dot2c_f32_f16_e32 v222, s43, v149
	v_and_b32_e32 v149, s32, v149
	v_dot2c_f32_f16_e32 v219, s43, v117
	v_dot2c_f32_f16_e32 v218, s43, v149
	v_perm_b32 v149, v171, v175, s29
	v_dot2c_f32_f16_e32 v216, s43, v149
	v_and_b32_e32 v149, s32, v149
	v_dot2c_f32_f16_e32 v212, s43, v149
	v_perm_b32 v149, v171, v175, s30
	v_dot2c_f32_f16_e32 v217, s43, v149
	v_and_b32_e32 v149, s32, v149
	v_dot2c_f32_f16_e32 v213, s43, v149
	v_perm_b32 v149, v171, v175, s31
	v_perm_b32 v117, v171, v175, s33
	v_dot2c_f32_f16_e32 v215, s43, v117
	v_and_b32_e32 v117, s32, v117
	v_dot2c_f32_f16_e32 v214, s43, v149
	v_and_b32_e32 v149, s32, v149
	v_dot2c_f32_f16_e32 v211, s43, v117
	v_dot2c_f32_f16_e32 v210, s43, v149
	v_perm_b32 v149, v162, v166, s29
	v_dot2c_f32_f16_e32 v224, s41, v149
	v_and_b32_e32 v149, s32, v149
	v_dot2c_f32_f16_e32 v220, s41, v149
	v_perm_b32 v149, v162, v166, s30
	v_dot2c_f32_f16_e32 v225, s41, v149
	v_and_b32_e32 v149, s32, v149
	v_dot2c_f32_f16_e32 v221, s41, v149
	v_perm_b32 v149, v162, v166, s31
	v_perm_b32 v117, v162, v166, s33
	v_dot2c_f32_f16_e32 v223, s41, v117
	v_and_b32_e32 v117, s32, v117
	v_dot2c_f32_f16_e32 v222, s41, v149
	v_and_b32_e32 v149, s32, v149
	v_dot2c_f32_f16_e32 v219, s41, v117
	v_dot2c_f32_f16_e32 v218, s41, v149
	v_perm_b32 v149, v163, v167, s29
	v_dot2c_f32_f16_e32 v216, s41, v149
	v_and_b32_e32 v149, s32, v149
	v_dot2c_f32_f16_e32 v212, s41, v149
	v_perm_b32 v149, v163, v167, s30
	v_dot2c_f32_f16_e32 v217, s41, v149
	v_and_b32_e32 v149, s32, v149
	v_dot2c_f32_f16_e32 v213, s41, v149
	v_perm_b32 v149, v163, v167, s31
	v_perm_b32 v117, v163, v167, s33
	v_dot2c_f32_f16_e32 v215, s41, v117
	v_and_b32_e32 v117, s32, v117
	v_dot2c_f32_f16_e32 v214, s41, v149
	v_and_b32_e32 v149, s32, v149
	v_dot2c_f32_f16_e32 v211, s41, v117
	v_dot2c_f32_f16_e32 v210, s41, v149
	v_perm_b32 v149, v154, v158, s29
	v_dot2c_f32_f16_e32 v224, s39, v149
	v_and_b32_e32 v149, s32, v149
	v_dot2c_f32_f16_e32 v220, s39, v149
	v_perm_b32 v149, v154, v158, s30
	v_dot2c_f32_f16_e32 v225, s39, v149
	v_and_b32_e32 v149, s32, v149
	v_dot2c_f32_f16_e32 v221, s39, v149
	v_perm_b32 v149, v154, v158, s31
	v_perm_b32 v117, v154, v158, s33
	v_dot2c_f32_f16_e32 v223, s39, v117
	v_and_b32_e32 v117, s32, v117
	v_dot2c_f32_f16_e32 v222, s39, v149
	v_and_b32_e32 v149, s32, v149
	v_dot2c_f32_f16_e32 v219, s39, v117
	v_dot2c_f32_f16_e32 v218, s39, v149
	v_perm_b32 v149, v155, v159, s29
	v_dot2c_f32_f16_e32 v216, s39, v149
	v_and_b32_e32 v149, s32, v149
	v_dot2c_f32_f16_e32 v212, s39, v149
	v_perm_b32 v149, v155, v159, s30
	v_dot2c_f32_f16_e32 v217, s39, v149
	v_and_b32_e32 v149, s32, v149
	v_dot2c_f32_f16_e32 v213, s39, v149
	v_perm_b32 v149, v155, v159, s31
	v_perm_b32 v117, v155, v159, s33
	v_dot2c_f32_f16_e32 v215, s39, v117
	v_and_b32_e32 v117, s32, v117
	v_dot2c_f32_f16_e32 v214, s39, v149
	v_and_b32_e32 v149, s32, v149
	v_dot2c_f32_f16_e32 v211, s39, v117
	v_perm_b32 v148, v146, v150, s29
	v_dot2c_f32_f16_e32 v224, s37, v148
	v_and_b32_e32 v148, s32, v148
	v_dot2c_f32_f16_e32 v220, s37, v148
	v_perm_b32 v148, v146, v150, s30
	v_dot2c_f32_f16_e32 v225, s37, v148
	v_and_b32_e32 v148, s32, v148
	v_dot2c_f32_f16_e32 v221, s37, v148
	v_perm_b32 v148, v146, v150, s31
	v_perm_b32 v117, v146, v150, s33
	v_dot2c_f32_f16_e32 v223, s37, v117
	v_and_b32_e32 v117, s32, v117
	v_dot2c_f32_f16_e32 v222, s37, v148
	v_and_b32_e32 v148, s32, v148
	v_dot2c_f32_f16_e32 v219, s37, v117
	v_perm_b32 v207, v147, v151, s29
	v_dot2c_f32_f16_e32 v216, s37, v207
	v_and_b32_e32 v207, s32, v207
	v_dot2c_f32_f16_e32 v212, s37, v207
	v_perm_b32 v207, v147, v151, s30
	v_dot2c_f32_f16_e32 v217, s37, v207
	v_and_b32_e32 v207, s32, v207
	v_dot2c_f32_f16_e32 v213, s37, v207
	v_perm_b32 v207, v147, v151, s31
	v_perm_b32 v117, v147, v151, s33
	v_dot2c_f32_f16_e32 v215, s37, v117
	v_and_b32_e32 v117, s32, v117
	v_dot2c_f32_f16_e32 v214, s37, v207
	v_and_b32_e32 v207, s32, v207
	v_dot2c_f32_f16_e32 v211, s37, v117
	v_perm_b32 v145, v114, v118, s29
	v_dot2c_f32_f16_e32 v224, s35, v145
	v_and_b32_e32 v145, s32, v145
	v_dot2c_f32_f16_e32 v220, s35, v145
	v_perm_b32 v145, v114, v118, s30
	v_dot2c_f32_f16_e32 v225, s35, v145
	v_and_b32_e32 v145, s32, v145
	v_dot2c_f32_f16_e32 v221, s35, v145
	v_perm_b32 v145, v114, v118, s31
	v_dot2c_f32_f16_e32 v222, s35, v145
	v_and_b32_e32 v145, s32, v145
	v_perm_b32 v117, v114, v118, s33
	v_and_b32_e32 v209, s32, v117
	v_dot2c_f32_f16_e32 v223, s35, v117
	v_dot2c_f32_f16_e32 v219, s35, v209
	v_perm_b32 v253, v115, v119, s29
	v_dot2c_f32_f16_e32 v216, s35, v253
	v_and_b32_e32 v253, s32, v253
	v_dot2c_f32_f16_e32 v212, s35, v253
	v_perm_b32 v253, v115, v119, s30
	v_dot2c_f32_f16_e32 v217, s35, v253
	v_and_b32_e32 v253, s32, v253
	v_dot2c_f32_f16_e32 v213, s35, v253
	v_perm_b32 v253, v115, v119, s31
	v_perm_b32 v209, v115, v119, s33
	v_dot2c_f32_f16_e32 v215, s35, v209
	v_and_b32_e32 v209, s32, v209
	v_dot2c_f32_f16_e32 v214, s35, v253
	v_and_b32_e32 v253, s32, v253
	v_dot2c_f32_f16_e32 v211, s35, v209
	v_perm_b32 v117, v68, v72, s29
	v_dot2c_f32_f16_e32 v224, s4, v117
	v_and_b32_e32 v117, s32, v117
	v_dot2c_f32_f16_e32 v220, s4, v117
	v_perm_b32 v117, v68, v72, s30
	v_dot2c_f32_f16_e32 v225, s4, v117
	v_and_b32_e32 v117, s32, v117
	v_dot2c_f32_f16_e32 v221, s4, v117
	v_perm_b32 v117, v68, v72, s31
	v_dot2c_f32_f16_e32 v222, s4, v117
	v_and_b32_e32 v117, s32, v117
	v_perm_b32 v254, v68, v72, s33
	v_and_b32_e32 v254, s32, v254
	v_perm_b32 v209, v68, v72, s33
	v_dot2c_f32_f16_e32 v219, s4, v254
	v_dot2c_f32_f16_e32 v223, s4, v209
	v_perm_b32 v209, v69, v73, s29
	v_dot2c_f32_f16_e32 v216, s4, v209
	v_and_b32_e32 v209, s32, v209
	v_dot2c_f32_f16_e32 v212, s4, v209
	v_perm_b32 v209, v69, v73, s30
	v_dot2c_f32_f16_e32 v217, s4, v209
	v_and_b32_e32 v209, s32, v209
	v_dot2c_f32_f16_e32 v213, s4, v209
	v_perm_b32 v209, v69, v73, s31
	v_perm_b32 v254, v69, v73, s33
	v_dot2c_f32_f16_e32 v215, s4, v254
	s_waitcnt vmcnt(31)
	v_dot8_i32_i4 v68, v248, v62, 0
	v_dot8_i32_i4 v68, v250, v63, v68
	v_dot2c_f32_f16_e32 v210, s39, v149
	v_dot2c_f32_f16_e32 v218, s37, v148
	v_dot2c_f32_f16_e32 v210, s37, v207
	v_lshlrev_b32_e32 v68, 4, v68
	v_dot8_i32_i4 v68, v247, v62, v68
	s_waitcnt vmcnt(30)
	v_dot8_i32_i4 v62, v248, v58, 0
	v_dot8_i32_i4 v62, v250, v59, v62
	v_dot8_i32_i4 v68, v249, v63, v68
	v_dot2c_f32_f16_e32 v218, s35, v145
	v_dot2c_f32_f16_e32 v210, s35, v253
	v_lshlrev_b32_e32 v62, 4, v62
	v_dot8_i32_i4 v62, v247, v58, v62
	s_waitcnt vmcnt(29)
	v_dot8_i32_i4 v58, v248, v54, 0
	v_dot8_i32_i4 v58, v250, v55, v58
	v_dot8_i32_i4 v62, v249, v59, v62
	v_dot2c_f32_f16_e32 v214, s4, v209
	v_and_b32_e32 v209, s32, v209
	v_lshlrev_b32_e32 v58, 4, v58
	v_dot8_i32_i4 v58, v247, v54, v58
	s_waitcnt vmcnt(28)
	v_dot8_i32_i4 v54, v248, v50, 0
	v_dot8_i32_i4 v54, v250, v51, v54
	v_dot8_i32_i4 v58, v249, v55, v58
	v_dot2c_f32_f16_e32 v218, s4, v117
	v_dot2c_f32_f16_e32 v210, s4, v209
	v_lshlrev_b32_e32 v54, 4, v54
	v_dot8_i32_i4 v54, v247, v50, v54
	s_waitcnt vmcnt(27)
	v_dot8_i32_i4 v50, v248, v46, 0
	v_dot8_i32_i4 v50, v250, v47, v50
	v_dot8_i32_i4 v54, v249, v51, v54
	s_add_i32 s24, s25, 2
	s_cmp_lt_u32 s25, 5
	v_lshlrev_b32_e32 v50, 4, v50
	v_dot8_i32_i4 v50, v247, v46, v50
	s_waitcnt vmcnt(26)
	v_dot8_i32_i4 v46, v248, v42, 0
	v_dot8_i32_i4 v46, v250, v43, v46
	v_dot8_i32_i4 v50, v249, v47, v50
	s_nop 0
	s_nop 0
	v_lshlrev_b32_e32 v46, 4, v46
	v_dot8_i32_i4 v46, v247, v42, v46
	s_waitcnt vmcnt(25)
	v_dot8_i32_i4 v42, v248, v38, 0
	v_dot8_i32_i4 v42, v250, v39, v42
	v_dot8_i32_i4 v46, v249, v43, v46
	s_nop 1
	v_lshlrev_b32_e32 v42, 4, v42
	v_dot8_i32_i4 v42, v247, v38, v42
	s_waitcnt vmcnt(24)
	v_dot8_i32_i4 v38, v248, v30, 0
	v_dot8_i32_i4 v38, v250, v31, v38
	v_dot8_i32_i4 v42, v249, v39, v42
	s_nop 1
	v_lshlrev_b32_e32 v38, 4, v38
	v_dot8_i32_i4 v38, v247, v30, v38
	v_dot8_i32_i4 v38, v249, v31, v38
	s_waitcnt vmcnt(22)
	v_dot8_i32_i4 v31, v248, v22, 0
	v_dot8_i32_i4 v31, v250, v23, v31
	v_dot8_i32_i4 v30, v248, v34, 0
	v_dot8_i32_i4 v30, v250, v35, v30
	s_nop 0
	v_lshlrev_b32_e32 v31, 4, v31
	v_dot8_i32_i4 v31, v247, v22, v31
	v_dot8_i32_i4 v31, v249, v23, v31
	s_waitcnt vmcnt(20)
	v_dot8_i32_i4 v23, v248, v14, 0
	v_dot8_i32_i4 v23, v250, v15, v23
	v_dot8_i32_i4 v22, v248, v26, 0
	v_dot8_i32_i4 v22, v250, v27, v22
	s_nop 0
	v_lshlrev_b32_e32 v23, 4, v23
	v_dot8_i32_i4 v23, v247, v14, v23
	v_dot8_i32_i4 v23, v249, v15, v23
	s_waitcnt vmcnt(18)
; __device__ __forceinline__ float gelu_as(float v) {
;     const float av = fabsf(v), t = __builtin_amdgcn_rcpf(av * 0.2316418882f + 1.0f);
;     float q = t * 0.5307027145f + (-0.7265760135f); q = q * t + 0.7107068705f; q = q * t + (-0.142248368f); q = q * t + 0.127414796f; q = q * t;
;     const float m = v * (q * __builtin_amdgcn_exp2f((v * v) * (-0.72134752044f)));
;     return v < 0.f ? m : v - m;
	v_dot8_i32_i4 v15, v248, v6, 0
	v_dot8_i32_i4 v15, v250, v7, v15
	v_dot8_i32_i4 v14, v248, v18, 0
	v_dot8_i32_i4 v14, v250, v19, v14
	s_nop 0
	v_lshlrev_b32_e32 v15, 4, v15
	v_dot8_i32_i4 v15, v247, v6, v15
	v_dot8_i32_i4 v15, v249, v7, v15
	s_waitcnt vmcnt(17)
	v_dot8_i32_i4 v6, v248, v10, 0
	s_waitcnt vmcnt(16)
	v_dot8_i32_i4 v7, v248, v2, 0
	v_dot8_i32_i4 v6, v250, v11, v6
	v_dot8_i32_i4 v7, v250, v3, v7
	v_lshlrev_b32_e32 v30, 4, v30
	v_lshlrev_b32_e32 v22, 4, v22
	v_lshlrev_b32_e32 v14, 4, v14
	v_lshlrev_b32_e32 v6, 4, v6
	v_lshlrev_b32_e32 v7, 4, v7
	v_dot8_i32_i4 v30, v247, v34, v30
	v_dot8_i32_i4 v22, v247, v26, v22
	v_dot8_i32_i4 v14, v247, v18, v14
	v_dot8_i32_i4 v6, v247, v10, v6
	v_dot8_i32_i4 v7, v247, v2, v7
	v_dot8_i32_i4 v30, v249, v35, v30
	v_dot8_i32_i4 v22, v249, v27, v22
	v_dot8_i32_i4 v14, v249, v19, v14
	v_dot8_i32_i4 v6, v249, v11, v6
	v_dot8_i32_i4 v7, v249, v3, v7
	v_permlane32_swap_b32_e32 v68, v30
	v_permlane32_swap_b32_e32 v62, v31
	v_permlane32_swap_b32_e32 v58, v22
	v_permlane32_swap_b32_e32 v54, v23
	v_permlane32_swap_b32_e32 v50, v14
	v_permlane32_swap_b32_e32 v46, v15
	v_permlane32_swap_b32_e32 v42, v6
	v_permlane32_swap_b32_e32 v38, v7
	v_add_u32_e32 v2, v68, v30
	v_add_u32_e32 v3, v62, v31
	v_add_u32_e32 v10, v58, v22
	v_add_u32_e32 v11, v54, v23
	v_add_u32_e32 v14, v50, v14
	v_add_u32_e32 v15, v46, v15
	v_add_u32_e32 v6, v42, v6
	v_add_u32_e32 v7, v38, v7
	v_permlane16_swap_b32_e32 v2, v14
	v_permlane16_swap_b32_e32 v3, v15
	v_permlane16_swap_b32_e32 v10, v6
	v_permlane16_swap_b32_e32 v11, v7
	v_add_u32_e32 v2, v2, v14
	v_add_u32_e32 v3, v3, v15
	v_add_u32_e32 v6, v10, v6
	v_add_u32_e32 v7, v11, v7
	v_cndmask_b32_e64 v10, v6, v2, s[0:1]
	v_cndmask_b32_e64 v2, v2, v6, s[0:1]
	v_cndmask_b32_e64 v6, v7, v3, s[0:1]
	v_cndmask_b32_e64 v3, v3, v7, s[0:1]
	v_add_u32_dpp v2, v2, v10 quad_perm:[2,3,0,1] row_mask:0xf bank_mask:0xf bound_ctrl:1
	s_waitcnt lgkmcnt(0)
	ds_read_b32 v7, v66 offset:1088
	v_add_u32_dpp v3, v3, v6 quad_perm:[2,3,0,1] row_mask:0xf bank_mask:0xf bound_ctrl:1
	v_cndmask_b32_e64 v6, v3, v2, s[2:3]
	v_cndmask_b32_e64 v2, v2, v3, s[2:3]
	ds_read_b32 v3, v66 offset:64
	v_add_f32_e32 v68, v252, v116
	v_add_u32_dpp v2, v2, v6 quad_perm:[1,0,3,2] row_mask:0xf bank_mask:0xf bound_ctrl:1
	v_and_b32_e32 v6, s32, v254
	v_dot2c_f32_f16_e32 v211, s4, v6
	v_add_u32_dpp v2, v2, v2 row_ror:8 row_mask:0xf bank_mask:0xf bound_ctrl:1
	ds_read_b32 v6, v66 offset:576
	s_nop 0
	v_add_u32_dpp v2, v2, v2 row_ror:4 row_mask:0xf bank_mask:0xf bound_ctrl:1
	v_cvt_f32_i32_e32 v2, v2
	v_add_f32_e32 v2, v251, v2
	v_mul_f32_e32 v2, v244, v2
	s_waitcnt lgkmcnt(1)
	v_mul_f32_e32 v2, v2, v3
	v_fma_f32 v3, |v2|, s28, 1.0
	v_rcp_f32_e32 v3, v3
	v_mul_f32_e32 v11, v2, v2
	v_mul_f32_e32 v11, 0xbf38aa3b, v11
	v_exp_f32_e32 v11, v11
	v_fmamk_f32 v10, v3, 0x3f07dc22, v227
	v_fmaak_f32 v10, v3, v10, 0x3f35f0e3
	v_fmaak_f32 v10, v3, v10, 0xbe11a98e
	v_fmaak_f32 v10, v3, v10, 0x3e027906
	v_mul_f32_e32 v3, v3, v10
	v_mul_f32_e32 v3, v11, v3
	v_mul_f32_e32 v10, v2, v3
	v_fma_f32 v3, -v2, v3, v2
	v_cmp_gt_f32_e64 s[4:5], 0, v2
	s_nop 1
	v_cndmask_b32_e64 v2, v3, v10, s[4:5]
	s_waitcnt lgkmcnt(0)
	v_mul_f32_e32 v2, v2, v6
	v_mul_f32_e32 v2, v2, v7
	s_cselect_b64 s[4:5], -1, 0
	s_nop 0
	v_mov_b32_dpp v253, v2 quad_perm:[1,0,3,2] row_mask:0xf bank_mask:0xf
	v_cvt_pk_f16_f32 v254, v2, v253
	v_cvt_f32_f16_e32 v66, v254
	v_readlane_b32 s5, v254, 0
	v_perm_b32 v14, v60, v64, s29
	s_nop 0
	v_dot2c_f32_f16_e32 v224, s5, v14
	v_and_b32_e32 v14, s32, v14
	v_dot2c_f32_f16_e32 v220, s5, v14
	v_perm_b32 v14, v60, v64, s30
	v_dot2c_f32_f16_e32 v225, s5, v14
	v_and_b32_e32 v14, s32, v14
	v_dot2c_f32_f16_e32 v221, s5, v14
	v_perm_b32 v14, v60, v64, s31
	v_perm_b32 v6, v60, v64, s33
	v_dot2c_f32_f16_e32 v223, s5, v6
	v_and_b32_e32 v6, s32, v6
	v_dot2c_f32_f16_e32 v222, s5, v14
	v_and_b32_e32 v14, s32, v14
	v_dot2c_f32_f16_e32 v219, s5, v6
	v_dot2c_f32_f16_e32 v218, s5, v14
	v_perm_b32 v14, v61, v65, s29
	v_dot2c_f32_f16_e32 v216, s5, v14
	v_and_b32_e32 v14, s32, v14
	v_dot2c_f32_f16_e32 v212, s5, v14
	v_perm_b32 v14, v61, v65, s30
	v_dot2c_f32_f16_e32 v217, s5, v14
	v_and_b32_e32 v14, s32, v14
	v_dot2c_f32_f16_e32 v213, s5, v14
	v_perm_b32 v14, v61, v65, s31
	v_perm_b32 v6, v61, v65, s33
	v_dot2c_f32_f16_e32 v214, s5, v14
	v_and_b32_e32 v14, s32, v14
	v_dot2c_f32_f16_e32 v215, s5, v6
	v_and_b32_e32 v6, s32, v6
	v_dot2c_f32_f16_e32 v210, s5, v14
	v_dot2c_f32_f16_e32 v211, s5, v6
	v_readlane_b32 s4, v254, 2
	buffer_load_dwordx4 v[62:65], v194, s[80:83], s64 offen
	buffer_load_dwordx4 v[58:61], v194, s[80:83], s65 offen
	v_perm_b32 v14, v52, v56, s29
	v_dot2c_f32_f16_e32 v224, s4, v14
	v_and_b32_e32 v14, s32, v14
	v_dot2c_f32_f16_e32 v220, s4, v14
	v_perm_b32 v14, v52, v56, s30
	v_dot2c_f32_f16_e32 v225, s4, v14
	v_and_b32_e32 v14, s32, v14
	v_dot2c_f32_f16_e32 v221, s4, v14
	v_perm_b32 v14, v52, v56, s31
	v_perm_b32 v6, v52, v56, s33
	v_dot2c_f32_f16_e32 v223, s4, v6
	v_and_b32_e32 v6, s32, v6
	v_dot2c_f32_f16_e32 v222, s4, v14
	v_and_b32_e32 v14, s32, v14
	v_dot2c_f32_f16_e32 v219, s4, v6
	v_dot2c_f32_f16_e32 v218, s4, v14
	v_perm_b32 v14, v53, v57, s29
	v_dot2c_f32_f16_e32 v216, s4, v14
	v_and_b32_e32 v14, s32, v14
	v_dot2c_f32_f16_e32 v212, s4, v14
	v_perm_b32 v14, v53, v57, s30
	v_dot2c_f32_f16_e32 v217, s4, v14
	v_and_b32_e32 v14, s32, v14
	v_dot2c_f32_f16_e32 v213, s4, v14
	v_perm_b32 v14, v53, v57, s31
	v_perm_b32 v6, v53, v57, s33
	v_dot2c_f32_f16_e32 v214, s4, v14
	v_and_b32_e32 v14, s32, v14
	v_dot2c_f32_f16_e32 v215, s4, v6
	v_and_b32_e32 v6, s32, v6
	v_dot2c_f32_f16_e32 v210, s4, v14
	v_dot2c_f32_f16_e32 v211, s4, v6
	v_readlane_b32 s4, v254, 16
	buffer_load_dwordx4 v[54:57], v194, s[80:83], s66 offen
	buffer_load_dwordx4 v[50:53], v194, s[80:83], s67 offen
	v_perm_b32 v14, v44, v48, s29
	v_dot2c_f32_f16_e32 v224, s4, v14
	v_and_b32_e32 v14, s32, v14
	v_dot2c_f32_f16_e32 v220, s4, v14
	v_perm_b32 v14, v44, v48, s30
	v_dot2c_f32_f16_e32 v225, s4, v14
	v_and_b32_e32 v14, s32, v14
	v_dot2c_f32_f16_e32 v221, s4, v14
	v_perm_b32 v14, v44, v48, s31
	v_perm_b32 v6, v44, v48, s33
	v_dot2c_f32_f16_e32 v223, s4, v6
	v_and_b32_e32 v6, s32, v6
	v_dot2c_f32_f16_e32 v222, s4, v14
	v_and_b32_e32 v14, s32, v14
	v_dot2c_f32_f16_e32 v219, s4, v6
	v_dot2c_f32_f16_e32 v218, s4, v14
	v_perm_b32 v14, v45, v49, s29
	v_dot2c_f32_f16_e32 v216, s4, v14
	v_and_b32_e32 v14, s32, v14
	v_dot2c_f32_f16_e32 v212, s4, v14
	v_perm_b32 v14, v45, v49, s30
	v_dot2c_f32_f16_e32 v217, s4, v14
	v_and_b32_e32 v14, s32, v14
	v_dot2c_f32_f16_e32 v213, s4, v14
	v_perm_b32 v14, v45, v49, s31
	v_perm_b32 v6, v45, v49, s33
	v_dot2c_f32_f16_e32 v214, s4, v14
	v_and_b32_e32 v14, s32, v14
	v_dot2c_f32_f16_e32 v215, s4, v6
	v_and_b32_e32 v6, s32, v6
	v_dot2c_f32_f16_e32 v210, s4, v14
	v_dot2c_f32_f16_e32 v211, s4, v6
	v_readlane_b32 s4, v254, 18
	buffer_load_dwordx4 v[46:49], v194, s[80:83], s68 offen
	buffer_load_dwordx4 v[42:45], v194, s[80:83], s69 offen
	v_perm_b32 v14, v32, v40, s29
	v_dot2c_f32_f16_e32 v224, s4, v14
	v_and_b32_e32 v14, s32, v14
	v_dot2c_f32_f16_e32 v220, s4, v14
	v_perm_b32 v14, v32, v40, s30
	v_dot2c_f32_f16_e32 v225, s4, v14
	v_and_b32_e32 v14, s32, v14
	v_dot2c_f32_f16_e32 v221, s4, v14
	v_perm_b32 v14, v32, v40, s31
	v_perm_b32 v6, v32, v40, s33
	v_dot2c_f32_f16_e32 v223, s4, v6
	v_and_b32_e32 v6, s32, v6
	v_dot2c_f32_f16_e32 v222, s4, v14
	v_and_b32_e32 v14, s32, v14
	v_dot2c_f32_f16_e32 v219, s4, v6
	v_dot2c_f32_f16_e32 v218, s4, v14
	v_perm_b32 v14, v33, v41, s29
	v_dot2c_f32_f16_e32 v216, s4, v14
	v_and_b32_e32 v14, s32, v14
	v_dot2c_f32_f16_e32 v212, s4, v14
	v_perm_b32 v14, v33, v41, s30
	v_dot2c_f32_f16_e32 v217, s4, v14
	v_and_b32_e32 v14, s32, v14
	v_dot2c_f32_f16_e32 v213, s4, v14
	v_perm_b32 v14, v33, v41, s31
	v_perm_b32 v6, v33, v41, s33
	v_dot2c_f32_f16_e32 v214, s4, v14
	v_and_b32_e32 v14, s32, v14
	v_dot2c_f32_f16_e32 v215, s4, v6
	v_and_b32_e32 v6, s32, v6
	v_dot2c_f32_f16_e32 v210, s4, v14
	v_dot2c_f32_f16_e32 v211, s4, v6
	v_readlane_b32 s4, v254, 32
	buffer_load_dwordx4 v[38:41], v194, s[80:83], s70 offen
	buffer_load_dwordx4 v[30:33], v194, s[80:83], s71 offen
	v_perm_b32 v14, v24, v36, s29
	v_dot2c_f32_f16_e32 v224, s4, v14
	v_and_b32_e32 v14, s32, v14
	v_dot2c_f32_f16_e32 v220, s4, v14
	v_perm_b32 v14, v24, v36, s30
	v_dot2c_f32_f16_e32 v225, s4, v14
	v_and_b32_e32 v14, s32, v14
	v_dot2c_f32_f16_e32 v221, s4, v14
	v_perm_b32 v14, v24, v36, s31
	v_perm_b32 v6, v24, v36, s33
	v_dot2c_f32_f16_e32 v223, s4, v6
	v_and_b32_e32 v6, s32, v6
	v_dot2c_f32_f16_e32 v222, s4, v14
	v_and_b32_e32 v14, s32, v14
	v_dot2c_f32_f16_e32 v219, s4, v6
	v_dot2c_f32_f16_e32 v218, s4, v14
	v_perm_b32 v14, v25, v37, s29
	v_dot2c_f32_f16_e32 v216, s4, v14
	v_and_b32_e32 v14, s32, v14
	v_dot2c_f32_f16_e32 v212, s4, v14
	v_perm_b32 v14, v25, v37, s30
	v_dot2c_f32_f16_e32 v217, s4, v14
	v_and_b32_e32 v14, s32, v14
	v_dot2c_f32_f16_e32 v213, s4, v14
	v_perm_b32 v14, v25, v37, s31
	v_perm_b32 v6, v25, v37, s33
	v_dot2c_f32_f16_e32 v214, s4, v14
	v_and_b32_e32 v14, s32, v14
	v_dot2c_f32_f16_e32 v215, s4, v6
	v_and_b32_e32 v6, s32, v6
	v_dot2c_f32_f16_e32 v210, s4, v14
	v_dot2c_f32_f16_e32 v211, s4, v6
	v_readlane_b32 s4, v254, 34
	buffer_load_dwordx4 v[34:37], v194, s[80:83], s72 offen
	buffer_load_dwordx4 v[22:25], v194, s[80:83], s73 offen
	v_perm_b32 v14, v16, v28, s29
	v_dot2c_f32_f16_e32 v224, s4, v14
	v_and_b32_e32 v14, s32, v14
	v_dot2c_f32_f16_e32 v220, s4, v14
	v_perm_b32 v14, v16, v28, s30
	v_dot2c_f32_f16_e32 v225, s4, v14
	v_and_b32_e32 v14, s32, v14
	v_dot2c_f32_f16_e32 v221, s4, v14
	v_perm_b32 v14, v16, v28, s31
	v_perm_b32 v6, v16, v28, s33
	v_dot2c_f32_f16_e32 v223, s4, v6
	v_and_b32_e32 v6, s32, v6
	v_dot2c_f32_f16_e32 v222, s4, v14
	v_and_b32_e32 v14, s32, v14
	v_dot2c_f32_f16_e32 v219, s4, v6
	v_dot2c_f32_f16_e32 v218, s4, v14
	v_perm_b32 v14, v17, v29, s29
	v_dot2c_f32_f16_e32 v216, s4, v14
	v_and_b32_e32 v14, s32, v14
; __device__ __forceinline__ void expert_tokens(const unsigned char* __restrict__ UV, const float* __restrict__ US, const float* __restrict__ VS, ...
;     ...
; #pragma unroll 1
;         for (int bi = 0; bi < 128 / EB; bi += 2) {
;             EXP_STEP(A, bi);
;             if (bi == 0) { nsu0 = US[ni0]; nsu1 = US[ni1]; nsv0 = VS[ni0]; nsv1 = VS[ni1]; }
;             EXP_STEP(B, bi + 1);
;         }
	v_dot2c_f32_f16_e32 v212, s4, v14
	v_perm_b32 v14, v17, v29, s30
	v_dot2c_f32_f16_e32 v217, s4, v14
	v_and_b32_e32 v14, s32, v14
	v_dot2c_f32_f16_e32 v213, s4, v14
	v_perm_b32 v14, v17, v29, s31
	v_perm_b32 v6, v17, v29, s33
	v_dot2c_f32_f16_e32 v214, s4, v14
	v_and_b32_e32 v14, s32, v14
	v_dot2c_f32_f16_e32 v215, s4, v6
	v_and_b32_e32 v6, s32, v6
	v_dot2c_f32_f16_e32 v210, s4, v14
	v_dot2c_f32_f16_e32 v211, s4, v6
	v_readlane_b32 s4, v254, 48
	buffer_load_dwordx4 v[26:29], v194, s[80:83], s74 offen
	buffer_load_dwordx4 v[14:17], v194, s[80:83], s75 offen
	v_perm_b32 v11, v8, v20, s29
	v_dot2c_f32_f16_e32 v224, s4, v11
	v_and_b32_e32 v11, s32, v11
	v_dot2c_f32_f16_e32 v220, s4, v11
	v_perm_b32 v11, v8, v20, s30
	v_dot2c_f32_f16_e32 v225, s4, v11
	v_and_b32_e32 v11, s32, v11
	v_dot2c_f32_f16_e32 v221, s4, v11
	v_perm_b32 v11, v8, v20, s31
	v_perm_b32 v6, v8, v20, s33
	v_dot2c_f32_f16_e32 v223, s4, v6
	v_and_b32_e32 v6, s32, v6
	v_dot2c_f32_f16_e32 v222, s4, v11
	v_and_b32_e32 v11, s32, v11
	v_dot2c_f32_f16_e32 v219, s4, v6
	v_perm_b32 v10, v9, v21, s29
	v_dot2c_f32_f16_e32 v216, s4, v10
	v_and_b32_e32 v10, s32, v10
	v_dot2c_f32_f16_e32 v212, s4, v10
	v_perm_b32 v10, v9, v21, s30
	v_dot2c_f32_f16_e32 v217, s4, v10
	v_and_b32_e32 v10, s32, v10
	v_dot2c_f32_f16_e32 v213, s4, v10
	v_perm_b32 v10, v9, v21, s31
	v_perm_b32 v6, v9, v21, s33
	v_dot2c_f32_f16_e32 v214, s4, v10
	v_and_b32_e32 v10, s32, v10
	v_dot2c_f32_f16_e32 v215, s4, v6
	v_and_b32_e32 v6, s32, v6
	v_dot2c_f32_f16_e32 v218, s4, v11
	v_dot2c_f32_f16_e32 v210, s4, v10
	v_dot2c_f32_f16_e32 v211, s4, v6
	v_readlane_b32 s4, v254, 50
	buffer_load_dwordx4 v[18:21], v194, s[80:83], s76 offen
	buffer_load_dwordx4 v[6:9], v194, s[80:83], s77 offen
	v_perm_b32 v254, v4, v12, s29
	v_dot2c_f32_f16_e32 v224, s4, v254
	v_and_b32_e32 v254, s32, v254
	v_dot2c_f32_f16_e32 v220, s4, v254
	v_perm_b32 v254, v4, v12, s30
	v_dot2c_f32_f16_e32 v225, s4, v254
	v_and_b32_e32 v254, s32, v254
	v_dot2c_f32_f16_e32 v221, s4, v254
	v_perm_b32 v254, v4, v12, s31
	v_perm_b32 v3, v4, v12, s33
	v_dot2c_f32_f16_e32 v223, s4, v3
	v_and_b32_e32 v3, s32, v3
	v_dot2c_f32_f16_e32 v222, s4, v254
	v_and_b32_e32 v254, s32, v254
	v_dot2c_f32_f16_e32 v219, s4, v3
	v_perm_b32 v11, v5, v13, s29
	v_dot2c_f32_f16_e32 v216, s4, v11
	v_and_b32_e32 v11, s32, v11
	v_dot2c_f32_f16_e32 v212, s4, v11
	v_perm_b32 v11, v5, v13, s30
	v_dot2c_f32_f16_e32 v217, s4, v11
	v_and_b32_e32 v11, s32, v11
	v_dot2c_f32_f16_e32 v213, s4, v11
	v_perm_b32 v11, v5, v13, s31
	v_perm_b32 v3, v5, v13, s33
	v_dot2c_f32_f16_e32 v214, s4, v11
	v_and_b32_e32 v11, s32, v11
	v_dot2c_f32_f16_e32 v215, s4, v3
	v_and_b32_e32 v3, s32, v3
	v_dot2c_f32_f16_e32 v218, s4, v254
	v_dot2c_f32_f16_e32 v210, s4, v11
	v_dot2c_f32_f16_e32 v211, s4, v3
	buffer_load_dwordx4 v[10:13], v194, s[80:83], s78 offen
	buffer_load_dwordx4 v[2:5], v194, s[80:83], s79 offen
	v_add_f32_e32 v252, v68, v66
	s_add_i32 s21, s21, 32
	s_and_b64 vcc, exec, s[22:23]
	s_cbranch_vccnz .LBB0_1013
	s_waitcnt vmcnt(16)
	v_mov_b64_e32 v[158:159], v[112:113]
	v_mov_b64_e32 v[190:191], v[80:81]
	v_mov_b64_e32 v[186:187], v[76:77]
	v_mov_b64_e32 v[182:183], v[88:89]
	v_mov_b64_e32 v[178:179], v[84:85]
	v_mov_b64_e32 v[174:175], v[96:97]
	v_mov_b64_e32 v[170:171], v[92:93]
	v_mov_b64_e32 v[166:167], v[104:105]
	v_mov_b64_e32 v[162:163], v[100:101]
	v_mov_b64_e32 v[156:157], v[110:111]
	v_mov_b64_e32 v[154:155], v[108:109]
	v_mov_b64_e32 v[150:151], v[126:127]
	v_mov_b64_e32 v[146:147], v[122:123]
	v_mov_b64_e32 v[116:117], v[132:133]
	v_mov_b64_e32 v[112:113], v[128:129]
	v_mov_b64_e32 v[70:71], v[140:141]
	v_mov_b64_e32 v[66:67], v[136:137]
	v_mov_b64_e32 v[188:189], v[78:79]
	v_mov_b64_e32 v[184:185], v[74:75]
	v_mov_b64_e32 v[180:181], v[86:87]
	v_mov_b64_e32 v[176:177], v[82:83]
	v_mov_b64_e32 v[172:173], v[94:95]
	v_mov_b64_e32 v[168:169], v[90:91]
	v_mov_b64_e32 v[164:165], v[102:103]
	v_mov_b64_e32 v[160:161], v[98:99]
	v_mov_b64_e32 v[152:153], v[106:107]
	v_mov_b64_e32 v[148:149], v[124:125]
	v_mov_b64_e32 v[144:145], v[120:121]
	v_mov_b64_e32 v[118:119], v[134:135]
	v_mov_b64_e32 v[114:115], v[130:131]
	v_mov_b64_e32 v[72:73], v[142:143]
	v_mov_b64_e32 v[68:69], v[138:139]
	s_mov_b32 s25, s24
	s_branch .LBB0_1019

; __device__ __forceinline__ void expert_tokens(const unsigned char* __restrict__ UV, const float* __restrict__ US, const float* __restrict__ VS, ...
;     ...
;         const unsigned nw0 = (unsigned)IDX[(size_t)tn * 128 + lane], nw1 = (unsigned)IDX[(size_t)tn * 128 + 64 + lane];
;         const int ni0 = (int)nw0 & rmask, ni1 = (int)nw1 & rmask;
;         const float ng0 = __uint_as_float(nw0 & 0xFFFF0000u), ng1 = __uint_as_float(nw1 & 0xFFFF0000u);
;     ...
;         ci0 = ni0; ci1 = ni1; cg0 = ng0; cg1 = ng1; csu0 = nsu0; csu1 = nsu1; csv0 = nsv0; csv1 = nsv1;
.LBB0_1024:
	s_waitcnt vmcnt(0)
	v_mul_f32_e32 v235, s16, v235
	v_mul_f32_e32 v236, s16, v236
	ds_write_b32 v232, v233
	ds_write_b32 v232, v234 offset:256
	ds_write_b32 v232, v235 offset:1024
	ds_write_b32 v232, v236 offset:1280
	v_and_b32_e32 v233, 0xffff0000, v229
	v_and_b32_e32 v234, 0xffff0000, v230
	ds_write_b32 v232, v233 offset:512
	ds_write_b32 v232, v234 offset:768
	s_andn2_b64 vcc, exec, s[22:23]
	s_cbranch_vccz .LBB0_1017
	s_branch .LBB0_1018
